# adds hand-written weight-conversion queue (4 items in flight per wave, ticket prefetch) with 224 GEMM workgroups in the in-projection phase
# speedup vs baseline: 1.0032x; 1.0032x over previous
.LBB0_74:
	s_load_dwordx16 s[8:23], s[0:1], 0x40
	v_writelane_b32 v254, s34, 10
	s_cmp_lt_i32 s30, 2
	s_cselect_b64 s[0:1], -1, 0
	v_writelane_b32 v254, s35, 11
	s_waitcnt lgkmcnt(0)
	v_writelane_b32 v254, s8, 12
	s_add_u32 s2, s28, 0x3300000
	s_addc_u32 s3, s29, 0
	v_writelane_b32 v254, s9, 13
	v_writelane_b32 v254, s10, 14
	v_writelane_b32 v254, s11, 15
	v_writelane_b32 v254, s12, 16
	v_writelane_b32 v254, s13, 17
	v_writelane_b32 v254, s14, 18
	v_writelane_b32 v254, s15, 19
	v_writelane_b32 v254, s16, 20
	v_writelane_b32 v254, s17, 21
	v_writelane_b32 v254, s18, 22
	v_writelane_b32 v254, s19, 23
	v_writelane_b32 v254, s20, 24
	v_writelane_b32 v254, s21, 25
	v_writelane_b32 v254, s22, 26
	v_writelane_b32 v254, s23, 27
	v_writelane_b32 v254, s2, 28
	s_nop 1
	v_writelane_b32 v254, s3, 29
	s_add_u32 s2, s28, 0x4300000
	s_addc_u32 s3, s29, 0
	v_writelane_b32 v254, s2, 30
	s_nop 1
	v_writelane_b32 v254, s3, 31
	s_add_u32 s2, s28, 0x5b00000
	s_addc_u32 s3, s29, 0
	v_writelane_b32 v254, s2, 32
	s_nop 1
	v_writelane_b32 v254, s3, 33
	s_add_u32 s2, s28, 0x6300000
	v_writelane_b32 v254, s2, 34
	s_addc_u32 s2, s29, 0
	v_writelane_b32 v254, s2, 35
	s_add_u32 s2, s28, 0x1e300000
	v_writelane_b32 v254, s2, 36
	s_addc_u32 s2, s29, 0
	s_add_u32 s36, s28, 0x2a300000
	s_addc_u32 s37, s29, 0
	s_add_u32 s96, s28, 0x36300000
	s_addc_u32 s97, s29, 0
	s_and_b64 s[4:5], s[0:1], s[4:5]
	v_writelane_b32 v254, s2, 37
	s_andn2_b64 vcc, exec, s[4:5]
	s_cbranch_vccnz .LBB0_231
	v_readlane_b32 s1, v254, 3
	s_sub_i32 s0, s1, 32
	s_cmpk_gt_i32 s1, 0x7f
	s_cselect_b32 s2, s0, s1
	s_cmp_lt_i32 s93, s2
	s_cbranch_scc1 .LBB0_77
	v_lshlrev_b32_e32 v146, 2, v0
	s_cbranch_execz .LBB0_78
	s_branch .LBB0_90

.LBB0_90:
	v_readlane_b32 s0, v254, 8
	s_lshl_b32 s0, s0, 14
	v_and_b32_e32 v1, 63, v0
	v_lshrrev_b32_e32 v233, 3, v1
	v_and_b32_e32 v235, 7, v1
	v_lshlrev_b32_e32 v234, 4, v235
	v_lshlrev_b32_e32 v178, 5, v235
	v_mul_u32_u24_e32 v1, 0x84, v233
	v_add3_u32 v180, v1, v234, s0
	v_add_u32_e32 v181, 0x420, v180
	v_add_u32_e32 v182, 0x420, v181
	v_add_u32_e32 v183, 0x420, v182
	v_add_u32_e32 v184, 0x420, v183
	v_add_u32_e32 v185, 0x420, v184
	v_add_u32_e32 v186, 0x420, v185
	v_add_u32_e32 v187, 0x420, v186
	v_mul_u32_u24_e32 v1, 0x420, v235
	v_lshlrev_b32_e32 v188, 2, v233
	v_add3_u32 v188, v1, v188, s0
	v_mov_b32_e32 v231, 1
	v_mov_b32_e32 v232, 0
	s_waitcnt vmcnt(0) lgkmcnt(0)
	s_barrier
	s_mov_b64 exec, 1
	global_atomic_add v230, v232, v231, s[28:29] offset:256 sc0
	s_mov_b64 exec, -1
	s_waitcnt vmcnt(0)
	v_readfirstlane_b32 s20, v230
	s_cmp_lt_u32 s20, 0x4e00
	s_cbranch_scc0 .Lq_exit
	s_mov_b64 exec, 1
	global_atomic_add v230, v232, v231, s[28:29] offset:256 sc0
	s_mov_b64 exec, -1
	s_lshl_b32 s21, s20, 3
	s_mov_b32 s17, 0
	v_readlane_b32 s8, v254, 12
	v_readlane_b32 s9, v254, 13
	s_mov_b32 s59, 0
	s_mov_b32 s58, 0
	s_cmp_lt_u32 s21, 0x1000
	s_cbranch_scc0 .Lq_p_n1
	s_lshr_b32 s22, s21, 6
	s_and_b32 s23, s21, 63
	s_mov_b32 s52, 0x800
	s_mov_b32 s53, 0x1000
	s_mov_b64 s[54:55], s[82:83]
	v_readlane_b32 s56, v254, 28
	v_readlane_b32 s57, v254, 29
	s_lshl_b32 s18, s23, 5
	s_branch .Lq_p_common
.Lq_p_n1:
	s_cmp_lt_u32 s21, 0x2000
	s_cbranch_scc0 .Lq_p_n2
	s_sub_u32 s19, s21, 0x1000
	s_lshr_b32 s22, s19, 7
	s_and_b32 s23, s19, 127
	s_mov_b32 s52, 0x1000
	s_mov_b32 s53, 0x800
	v_readlane_b32 s54, v254, 14
	v_readlane_b32 s55, v254, 15
	v_readlane_b32 s56, v254, 30
	v_readlane_b32 s57, v254, 31
	s_lshl_b32 s18, s23, 5
	s_mov_b32 s17, 2
	s_mov_b32 s59, 1
	s_branch .Lq_p_common
.Lq_p_n2:
	s_cmp_lt_u32 s21, 0x2800
	s_cbranch_scc0 .Lq_p_n3
	s_sub_u32 s19, s21, 0x2000
	s_lshr_b32 s22, s19, 6
	s_and_b32 s23, s19, 63
	s_mov_b32 s52, 0x800
	s_mov_b32 s53, 0x800
	v_readlane_b32 s54, v254, 20
	v_readlane_b32 s55, v254, 21
	v_readlane_b32 s56, v254, 30
	v_readlane_b32 s57, v254, 31
	s_lshl_b32 s18, s23, 5
	s_add_u32 s18, s18, 0x1000
	v_readlane_b32 s8, v254, 18
	v_readlane_b32 s9, v254, 19
	s_mov_b32 s17, 2
	s_mov_b32 s59, 1
	s_branch .Lq_p_common
.Lq_p_n3:
	s_cmp_lt_u32 s21, 0x3000
	s_cbranch_scc0 .Lq_p_n4
	s_sub_u32 s19, s21, 0x2800
	s_lshr_b32 s22, s19, 6
	s_and_b32 s23, s19, 63
	s_mov_b32 s52, 0x800
	s_mov_b32 s53, 0x800
	v_readlane_b32 s54, v254, 24
	v_readlane_b32 s55, v254, 25
	v_readlane_b32 s56, v254, 32
	v_readlane_b32 s57, v254, 33
	s_lshl_b32 s18, s23, 5
	s_branch .Lq_p_common
.Lq_p_n4:
	s_cmp_lt_u32 s21, 0x1b000
	s_cbranch_scc0 .Lq_p_dn
	s_cmp_lt_u32 s21, 0xf000
	s_cbranch_scc0 .Lq_p_up
	s_sub_u32 s19, s21, 0x3000
	s_mov_b64 s[54:55], s[44:45]
	s_branch .Lq_p_gu
.Lq_p_up:
	s_sub_u32 s19, s21, 0xf000
	s_mov_b64 s[54:55], s[46:47]
	s_mov_b32 s58, 0x80
.Lq_p_gu:
	s_lshr_b32 s2, s19, 8
	s_mul_i32 s2, s2, 0xaaab
	s_lshr_b32 s2, s2, 17
	s_mul_i32 s3, s2, 0x300
	s_sub_u32 s19, s19, s3
	s_lshr_b32 s22, s19, 3
	s_mul_i32 s22, s22, 0xaaab
	s_lshr_b32 s22, s22, 17
	s_mul_i32 s3, s22, 24
	s_sub_u32 s23, s19, s3
	s_mov_b32 s52, 0x300
	s_mov_b32 s53, 0x800
	s_mul_i32 s3, s2, 0x600000
	s_add_u32 s54, s54, s3
	s_addc_u32 s55, s55, 0
	v_readlane_b32 s56, v254, 34
	v_readlane_b32 s57, v254, 35
	s_add_u32 s56, s56, s3
	s_addc_u32 s57, s57, 0
	s_lshl_b32 s3, s23, 5
	s_lshr_b32 s18, s3, 7
	s_lshl_b32 s18, s18, 8
	s_and_b32 s3, s3, 127
	s_add_u32 s18, s18, s3
	s_add_u32 s18, s18, s58
	s_mov_b32 s17, 1
	s_branch .Lq_p_common
.Lq_p_dn:
	s_sub_u32 s19, s21, 0x1b000
	s_lshr_b32 s2, s19, 8
	s_mul_i32 s2, s2, 0xaaab
	s_lshr_b32 s2, s2, 17
	s_mul_i32 s3, s2, 0x300
	s_sub_u32 s19, s19, s3
	s_lshr_b32 s22, s19, 6
	s_and_b32 s23, s19, 63
	s_mov_b32 s52, 0x800
	s_mov_b32 s53, 0x300
	s_mul_i32 s3, s2, 0x600000
	s_add_u32 s54, s48, s3
	s_addc_u32 s55, s49, 0
	s_mul_i32 s3, s2, 0x300000
	v_readlane_b32 s56, v254, 36
	v_readlane_b32 s57, v254, 37
	s_add_u32 s56, s56, s3
	s_addc_u32 s57, s57, 0
	s_lshl_b32 s18, s23, 5
.Lq_p_common:
	s_lshl_b32 s2, s52, 8
	s_mul_i32 s3, s22, s2
	s_lshl_b32 s2, s23, 7
	s_add_u32 s3, s3, s2
	s_add_u32 s6, s54, s3
	s_addc_u32 s7, s55, 0
	s_lshl_b32 s2, s53, 1
	s_mul_i32 s3, s18, s2
	s_lshl_b32 s2, s22, 7
	s_add_u32 s3, s3, s2
	s_add_u32 s14, s56, s3
	s_addc_u32 s15, s57, 0
	s_lshl_b32 s16, s53, 6
	s_mul_i32 s2, s22, s59
	s_lshl_b32 s2, s2, 8
	s_add_u32 s8, s8, s2
	s_addc_u32 s9, s9, 0
	s_lshl_b32 s2, s52, 2
	v_mul_u32_u24_e32 v235, s2, v233
	v_add_u32_e32 v162, v235, v234
	s_lshl_b32 s2, s52, 5
	v_add_u32_e32 v163, s2, v162
	v_add_u32_e32 v164, s2, v163
	v_add_u32_e32 v165, s2, v164
	v_add_u32_e32 v166, s2, v165
	v_add_u32_e32 v167, s2, v166
	v_add_u32_e32 v168, s2, v167
	v_add_u32_e32 v169, s2, v168
	s_lshl_b32 s2, s53, 1
	v_mul_u32_u24_e32 v235, s2, v233
	v_add_u32_e32 v174, v235, v234
	s_lshl_b32 s2, s53, 4
	v_add_u32_e32 v175, s2, v174
	v_add_u32_e32 v176, s2, v175
	v_add_u32_e32 v177, s2, v176
	s_mov_b64 s[10:11], s[14:15]
	s_mov_b32 s12, s16
	s_mov_b32 s13, s17
	v_mov_b32_e32 v170, v174
	v_mov_b32_e32 v171, v175
	v_mov_b32_e32 v172, v176
	v_mov_b32_e32 v173, v177
	s_mov_b64 s[18:19], s[6:7]
	s_nop 1
	global_load_dwordx4 v[2:5], v162, s[18:19] nt
	global_load_dwordx4 v[6:9], v163, s[18:19] nt
	global_load_dwordx4 v[10:13], v164, s[18:19] nt
	global_load_dwordx4 v[14:17], v165, s[18:19] nt
	global_load_dwordx4 v[18:21], v166, s[18:19] nt
	global_load_dwordx4 v[22:25], v167, s[18:19] nt
	global_load_dwordx4 v[26:29], v168, s[18:19] nt
	global_load_dwordx4 v[30:33], v169, s[18:19] nt
	global_load_dwordx4 v[130:133], v178, s[8:9]
	global_load_dwordx4 v[134:137], v178, s[8:9] offset:16
	s_add_u32 s18, s6, 128
	s_addc_u32 s19, s7, 0
	s_nop 1
	global_load_dwordx4 v[34:37], v162, s[18:19] nt
	global_load_dwordx4 v[38:41], v163, s[18:19] nt
	global_load_dwordx4 v[42:45], v164, s[18:19] nt
	global_load_dwordx4 v[46:49], v165, s[18:19] nt
	global_load_dwordx4 v[50:53], v166, s[18:19] nt
	global_load_dwordx4 v[54:57], v167, s[18:19] nt
	global_load_dwordx4 v[58:61], v168, s[18:19] nt
	global_load_dwordx4 v[62:65], v169, s[18:19] nt
	global_load_dwordx4 v[138:141], v178, s[8:9]
	global_load_dwordx4 v[142:145], v178, s[8:9] offset:16
	s_add_u32 s18, s6, 256
	s_addc_u32 s19, s7, 0
	s_nop 1
	global_load_dwordx4 v[66:69], v162, s[18:19] nt
	global_load_dwordx4 v[70:73], v163, s[18:19] nt
	global_load_dwordx4 v[74:77], v164, s[18:19] nt
	global_load_dwordx4 v[78:81], v165, s[18:19] nt
	global_load_dwordx4 v[82:85], v166, s[18:19] nt
	global_load_dwordx4 v[86:89], v167, s[18:19] nt
	global_load_dwordx4 v[90:93], v168, s[18:19] nt
	global_load_dwordx4 v[94:97], v169, s[18:19] nt
	global_load_dwordx4 v[146:149], v178, s[8:9]
	global_load_dwordx4 v[150:153], v178, s[8:9] offset:16
	s_add_u32 s18, s6, 384
	s_addc_u32 s19, s7, 0
	s_nop 1
	global_load_dwordx4 v[98:101], v162, s[18:19] nt
	global_load_dwordx4 v[102:105], v163, s[18:19] nt
	global_load_dwordx4 v[106:109], v164, s[18:19] nt
	global_load_dwordx4 v[110:113], v165, s[18:19] nt
	global_load_dwordx4 v[114:117], v166, s[18:19] nt
	global_load_dwordx4 v[118:121], v167, s[18:19] nt
	global_load_dwordx4 v[122:125], v168, s[18:19] nt
	global_load_dwordx4 v[126:129], v169, s[18:19] nt
	global_load_dwordx4 v[154:157], v178, s[8:9]
	global_load_dwordx4 v[158:161], v178, s[8:9] offset:16
	s_bitcmp1_b32 s13, 0
	s_cselect_b32 s2, 0, 0
	s_mul_i32 s2, s2, s12
	s_add_u32 s18, s10, s2
	s_addc_u32 s19, s11, 0
	s_waitcnt vmcnt(39)
	ds_write2_b32 v180, v2, v3 offset1:1
	ds_write2_b32 v180, v4, v5 offset0:2 offset1:3
	s_waitcnt vmcnt(38)
	ds_write2_b32 v181, v6, v7 offset1:1
	ds_write2_b32 v181, v8, v9 offset0:2 offset1:3
	s_waitcnt vmcnt(37)
	ds_write2_b32 v182, v10, v11 offset1:1
	ds_write2_b32 v182, v12, v13 offset0:2 offset1:3
	s_waitcnt vmcnt(36)
	ds_write2_b32 v183, v14, v15 offset1:1
	ds_write2_b32 v183, v16, v17 offset0:2 offset1:3
	s_waitcnt vmcnt(35)
	ds_write2_b32 v184, v18, v19 offset1:1
	ds_write2_b32 v184, v20, v21 offset0:2 offset1:3
	s_waitcnt vmcnt(34)
	ds_write2_b32 v185, v22, v23 offset1:1
	ds_write2_b32 v185, v24, v25 offset0:2 offset1:3
	s_waitcnt vmcnt(33)
	ds_write2_b32 v186, v26, v27 offset1:1
	ds_write2_b32 v186, v28, v29 offset0:2 offset1:3
	s_waitcnt vmcnt(32)
	ds_write2_b32 v187, v30, v31 offset1:1
	ds_write2_b32 v187, v32, v33 offset0:2 offset1:3
	s_waitcnt lgkmcnt(0)
	ds_read2_b32 v[190:191], v188 offset0:0 offset1:8
	ds_read2_b32 v[192:193], v188 offset0:33 offset1:41
	ds_read2_b32 v[194:195], v188 offset0:66 offset1:74
	ds_read2_b32 v[196:197], v188 offset0:99 offset1:107
	ds_read2_b32 v[198:199], v188 offset0:132 offset1:140
	ds_read2_b32 v[200:201], v188 offset0:165 offset1:173
	ds_read2_b32 v[202:203], v188 offset0:198 offset1:206
	ds_read2_b32 v[204:205], v188 offset0:231 offset1:239
	ds_read2_b32 v[206:207], v188 offset0:16 offset1:24
	ds_read2_b32 v[208:209], v188 offset0:49 offset1:57
	ds_read2_b32 v[210:211], v188 offset0:82 offset1:90
	ds_read2_b32 v[212:213], v188 offset0:115 offset1:123
	ds_read2_b32 v[214:215], v188 offset0:148 offset1:156
	ds_read2_b32 v[216:217], v188 offset0:181 offset1:189
	ds_read2_b32 v[218:219], v188 offset0:214 offset1:222
	ds_read2_b32 v[220:221], v188 offset0:247 offset1:255
	s_bitcmp1_b32 s13, 1
	s_cbranch_scc0 .Lq_ng_0
	s_waitcnt vmcnt(30)
	s_waitcnt lgkmcnt(0)
	v_mul_f32_e32 v190, v190, v130
	v_mul_f32_e32 v191, v191, v130
	v_mul_f32_e32 v206, v206, v130
	v_mul_f32_e32 v207, v207, v130
	v_mul_f32_e32 v192, v192, v131
	v_mul_f32_e32 v193, v193, v131
	v_mul_f32_e32 v208, v208, v131
	v_mul_f32_e32 v209, v209, v131
	v_mul_f32_e32 v194, v194, v132
	v_mul_f32_e32 v195, v195, v132
	v_mul_f32_e32 v210, v210, v132
	v_mul_f32_e32 v211, v211, v132
	v_mul_f32_e32 v196, v196, v133
	v_mul_f32_e32 v197, v197, v133
	v_mul_f32_e32 v212, v212, v133
	v_mul_f32_e32 v213, v213, v133
	v_mul_f32_e32 v198, v198, v134
	v_mul_f32_e32 v199, v199, v134
	v_mul_f32_e32 v214, v214, v134
	v_mul_f32_e32 v215, v215, v134
	v_mul_f32_e32 v200, v200, v135
	v_mul_f32_e32 v201, v201, v135
	v_mul_f32_e32 v216, v216, v135
	v_mul_f32_e32 v217, v217, v135
	v_mul_f32_e32 v202, v202, v136
	v_mul_f32_e32 v203, v203, v136
	v_mul_f32_e32 v218, v218, v136
	v_mul_f32_e32 v219, v219, v136
	v_mul_f32_e32 v204, v204, v137
	v_mul_f32_e32 v205, v205, v137
	v_mul_f32_e32 v220, v220, v137
	v_mul_f32_e32 v221, v221, v137
.Lq_ng_0:
	s_waitcnt lgkmcnt(14)
	v_cvt_pk_bf16_f32 v222, v190, v192
	s_waitcnt lgkmcnt(12)
	v_cvt_pk_bf16_f32 v223, v194, v196
	s_waitcnt lgkmcnt(10)
	v_cvt_pk_bf16_f32 v224, v198, v200
	s_waitcnt lgkmcnt(8)
	v_cvt_pk_bf16_f32 v225, v202, v204
	global_store_dwordx4 v170, v[222:225], s[18:19] nt
	v_cvt_pk_bf16_f32 v226, v191, v193
	v_cvt_pk_bf16_f32 v227, v195, v197
	v_cvt_pk_bf16_f32 v228, v199, v201
	v_cvt_pk_bf16_f32 v229, v203, v205
	global_store_dwordx4 v171, v[226:229], s[18:19] nt
	s_waitcnt lgkmcnt(6)
	v_cvt_pk_bf16_f32 v222, v206, v208
	s_waitcnt lgkmcnt(4)
	v_cvt_pk_bf16_f32 v223, v210, v212
	s_waitcnt lgkmcnt(2)
	v_cvt_pk_bf16_f32 v224, v214, v216
	s_waitcnt lgkmcnt(0)
	v_cvt_pk_bf16_f32 v225, v218, v220
	global_store_dwordx4 v172, v[222:225], s[18:19] nt
	v_cvt_pk_bf16_f32 v226, v207, v209
	v_cvt_pk_bf16_f32 v227, v211, v213
	v_cvt_pk_bf16_f32 v228, v215, v217
	v_cvt_pk_bf16_f32 v229, v219, v221
	global_store_dwordx4 v173, v[226:229], s[18:19] nt
	s_add_u32 s18, s6, 512
	s_addc_u32 s19, s7, 0
	s_nop 1
	global_load_dwordx4 v[2:5], v162, s[18:19] nt
	global_load_dwordx4 v[6:9], v163, s[18:19] nt
	global_load_dwordx4 v[10:13], v164, s[18:19] nt
	global_load_dwordx4 v[14:17], v165, s[18:19] nt
	global_load_dwordx4 v[18:21], v166, s[18:19] nt
	global_load_dwordx4 v[22:25], v167, s[18:19] nt
	global_load_dwordx4 v[26:29], v168, s[18:19] nt
	global_load_dwordx4 v[30:33], v169, s[18:19] nt
	global_load_dwordx4 v[130:133], v178, s[8:9]
	global_load_dwordx4 v[134:137], v178, s[8:9] offset:16
	s_bitcmp1_b32 s13, 0
	s_cselect_b32 s2, 1, 1
	s_mul_i32 s2, s2, s12
	s_add_u32 s18, s10, s2
	s_addc_u32 s19, s11, 0
	s_waitcnt vmcnt(43)
	ds_write2_b32 v180, v34, v35 offset1:1
	ds_write2_b32 v180, v36, v37 offset0:2 offset1:3
	s_waitcnt vmcnt(42)
	ds_write2_b32 v181, v38, v39 offset1:1
	ds_write2_b32 v181, v40, v41 offset0:2 offset1:3
	s_waitcnt vmcnt(41)
	ds_write2_b32 v182, v42, v43 offset1:1
	ds_write2_b32 v182, v44, v45 offset0:2 offset1:3
	s_waitcnt vmcnt(40)
	ds_write2_b32 v183, v46, v47 offset1:1
	ds_write2_b32 v183, v48, v49 offset0:2 offset1:3
	s_waitcnt vmcnt(39)
	ds_write2_b32 v184, v50, v51 offset1:1
	ds_write2_b32 v184, v52, v53 offset0:2 offset1:3
	s_waitcnt vmcnt(38)
	ds_write2_b32 v185, v54, v55 offset1:1
	ds_write2_b32 v185, v56, v57 offset0:2 offset1:3
	s_waitcnt vmcnt(37)
	ds_write2_b32 v186, v58, v59 offset1:1
	ds_write2_b32 v186, v60, v61 offset0:2 offset1:3
	s_waitcnt vmcnt(36)
	ds_write2_b32 v187, v62, v63 offset1:1
	ds_write2_b32 v187, v64, v65 offset0:2 offset1:3
	s_waitcnt lgkmcnt(0)
	ds_read2_b32 v[190:191], v188 offset0:0 offset1:8
	ds_read2_b32 v[192:193], v188 offset0:33 offset1:41
	ds_read2_b32 v[194:195], v188 offset0:66 offset1:74
	ds_read2_b32 v[196:197], v188 offset0:99 offset1:107
	ds_read2_b32 v[198:199], v188 offset0:132 offset1:140
	ds_read2_b32 v[200:201], v188 offset0:165 offset1:173
	ds_read2_b32 v[202:203], v188 offset0:198 offset1:206
	ds_read2_b32 v[204:205], v188 offset0:231 offset1:239
	ds_read2_b32 v[206:207], v188 offset0:16 offset1:24
	ds_read2_b32 v[208:209], v188 offset0:49 offset1:57
	ds_read2_b32 v[210:211], v188 offset0:82 offset1:90
	ds_read2_b32 v[212:213], v188 offset0:115 offset1:123
	ds_read2_b32 v[214:215], v188 offset0:148 offset1:156
	ds_read2_b32 v[216:217], v188 offset0:181 offset1:189
	ds_read2_b32 v[218:219], v188 offset0:214 offset1:222
	ds_read2_b32 v[220:221], v188 offset0:247 offset1:255
	s_bitcmp1_b32 s13, 1
	s_cbranch_scc0 .Lq_ng_1
	s_waitcnt vmcnt(34)
	s_waitcnt lgkmcnt(0)
	v_mul_f32_e32 v190, v190, v138
	v_mul_f32_e32 v191, v191, v138
	v_mul_f32_e32 v206, v206, v138
	v_mul_f32_e32 v207, v207, v138
	v_mul_f32_e32 v192, v192, v139
	v_mul_f32_e32 v193, v193, v139
	v_mul_f32_e32 v208, v208, v139
	v_mul_f32_e32 v209, v209, v139
	v_mul_f32_e32 v194, v194, v140
	v_mul_f32_e32 v195, v195, v140
	v_mul_f32_e32 v210, v210, v140
	v_mul_f32_e32 v211, v211, v140
	v_mul_f32_e32 v196, v196, v141
	v_mul_f32_e32 v197, v197, v141
	v_mul_f32_e32 v212, v212, v141
	v_mul_f32_e32 v213, v213, v141
	v_mul_f32_e32 v198, v198, v142
	v_mul_f32_e32 v199, v199, v142
	v_mul_f32_e32 v214, v214, v142
	v_mul_f32_e32 v215, v215, v142
	v_mul_f32_e32 v200, v200, v143
	v_mul_f32_e32 v201, v201, v143
	v_mul_f32_e32 v216, v216, v143
	v_mul_f32_e32 v217, v217, v143
	v_mul_f32_e32 v202, v202, v144
	v_mul_f32_e32 v203, v203, v144
	v_mul_f32_e32 v218, v218, v144
	v_mul_f32_e32 v219, v219, v144
	v_mul_f32_e32 v204, v204, v145
	v_mul_f32_e32 v205, v205, v145
	v_mul_f32_e32 v220, v220, v145
	v_mul_f32_e32 v221, v221, v145
.Lq_ng_1:
	s_waitcnt lgkmcnt(14)
	v_cvt_pk_bf16_f32 v222, v190, v192
	s_waitcnt lgkmcnt(12)
	v_cvt_pk_bf16_f32 v223, v194, v196
	s_waitcnt lgkmcnt(10)
	v_cvt_pk_bf16_f32 v224, v198, v200
	s_waitcnt lgkmcnt(8)
	v_cvt_pk_bf16_f32 v225, v202, v204
	global_store_dwordx4 v170, v[222:225], s[18:19] nt
	v_cvt_pk_bf16_f32 v226, v191, v193
	v_cvt_pk_bf16_f32 v227, v195, v197
	v_cvt_pk_bf16_f32 v228, v199, v201
	v_cvt_pk_bf16_f32 v229, v203, v205
	global_store_dwordx4 v171, v[226:229], s[18:19] nt
	s_waitcnt lgkmcnt(6)
	v_cvt_pk_bf16_f32 v222, v206, v208
	s_waitcnt lgkmcnt(4)
	v_cvt_pk_bf16_f32 v223, v210, v212
	s_waitcnt lgkmcnt(2)
	v_cvt_pk_bf16_f32 v224, v214, v216
	s_waitcnt lgkmcnt(0)
	v_cvt_pk_bf16_f32 v225, v218, v220
	global_store_dwordx4 v172, v[222:225], s[18:19] nt
	v_cvt_pk_bf16_f32 v226, v207, v209
	v_cvt_pk_bf16_f32 v227, v211, v213
	v_cvt_pk_bf16_f32 v228, v215, v217
	v_cvt_pk_bf16_f32 v229, v219, v221
	global_store_dwordx4 v173, v[226:229], s[18:19] nt
	s_add_u32 s18, s6, 640
	s_addc_u32 s19, s7, 0
	s_nop 1
	global_load_dwordx4 v[34:37], v162, s[18:19] nt
	global_load_dwordx4 v[38:41], v163, s[18:19] nt
	global_load_dwordx4 v[42:45], v164, s[18:19] nt
	global_load_dwordx4 v[46:49], v165, s[18:19] nt
	global_load_dwordx4 v[50:53], v166, s[18:19] nt
	global_load_dwordx4 v[54:57], v167, s[18:19] nt
	global_load_dwordx4 v[58:61], v168, s[18:19] nt
	global_load_dwordx4 v[62:65], v169, s[18:19] nt
	global_load_dwordx4 v[138:141], v178, s[8:9]
	global_load_dwordx4 v[142:145], v178, s[8:9] offset:16
	s_bitcmp1_b32 s13, 0
	s_cselect_b32 s2, 2, 2
	s_mul_i32 s2, s2, s12
	s_add_u32 s18, s10, s2
	s_addc_u32 s19, s11, 0
	s_waitcnt vmcnt(47)
	ds_write2_b32 v180, v66, v67 offset1:1
	ds_write2_b32 v180, v68, v69 offset0:2 offset1:3
	s_waitcnt vmcnt(46)
	ds_write2_b32 v181, v70, v71 offset1:1
	ds_write2_b32 v181, v72, v73 offset0:2 offset1:3
	s_waitcnt vmcnt(45)
	ds_write2_b32 v182, v74, v75 offset1:1
	ds_write2_b32 v182, v76, v77 offset0:2 offset1:3
	s_waitcnt vmcnt(44)
	ds_write2_b32 v183, v78, v79 offset1:1
	ds_write2_b32 v183, v80, v81 offset0:2 offset1:3
	s_waitcnt vmcnt(43)
	ds_write2_b32 v184, v82, v83 offset1:1
	ds_write2_b32 v184, v84, v85 offset0:2 offset1:3
	s_waitcnt vmcnt(42)
	ds_write2_b32 v185, v86, v87 offset1:1
	ds_write2_b32 v185, v88, v89 offset0:2 offset1:3
	s_waitcnt vmcnt(41)
	ds_write2_b32 v186, v90, v91 offset1:1
	ds_write2_b32 v186, v92, v93 offset0:2 offset1:3
	s_waitcnt vmcnt(40)
	ds_write2_b32 v187, v94, v95 offset1:1
	ds_write2_b32 v187, v96, v97 offset0:2 offset1:3
	s_waitcnt lgkmcnt(0)
	ds_read2_b32 v[190:191], v188 offset0:0 offset1:8
	ds_read2_b32 v[192:193], v188 offset0:33 offset1:41
	ds_read2_b32 v[194:195], v188 offset0:66 offset1:74
	ds_read2_b32 v[196:197], v188 offset0:99 offset1:107
	ds_read2_b32 v[198:199], v188 offset0:132 offset1:140
	ds_read2_b32 v[200:201], v188 offset0:165 offset1:173
	ds_read2_b32 v[202:203], v188 offset0:198 offset1:206
	ds_read2_b32 v[204:205], v188 offset0:231 offset1:239
	ds_read2_b32 v[206:207], v188 offset0:16 offset1:24
	ds_read2_b32 v[208:209], v188 offset0:49 offset1:57
	ds_read2_b32 v[210:211], v188 offset0:82 offset1:90
	ds_read2_b32 v[212:213], v188 offset0:115 offset1:123
	ds_read2_b32 v[214:215], v188 offset0:148 offset1:156
	ds_read2_b32 v[216:217], v188 offset0:181 offset1:189
	ds_read2_b32 v[218:219], v188 offset0:214 offset1:222
	ds_read2_b32 v[220:221], v188 offset0:247 offset1:255
	s_bitcmp1_b32 s13, 1
	s_cbranch_scc0 .Lq_ng_2
	s_waitcnt vmcnt(38)
	s_waitcnt lgkmcnt(0)
	v_mul_f32_e32 v190, v190, v146
	v_mul_f32_e32 v191, v191, v146
	v_mul_f32_e32 v206, v206, v146
	v_mul_f32_e32 v207, v207, v146
	v_mul_f32_e32 v192, v192, v147
	v_mul_f32_e32 v193, v193, v147
	v_mul_f32_e32 v208, v208, v147
	v_mul_f32_e32 v209, v209, v147
	v_mul_f32_e32 v194, v194, v148
	v_mul_f32_e32 v195, v195, v148
	v_mul_f32_e32 v210, v210, v148
	v_mul_f32_e32 v211, v211, v148
	v_mul_f32_e32 v196, v196, v149
	v_mul_f32_e32 v197, v197, v149
	v_mul_f32_e32 v212, v212, v149
	v_mul_f32_e32 v213, v213, v149
	v_mul_f32_e32 v198, v198, v150
	v_mul_f32_e32 v199, v199, v150
	v_mul_f32_e32 v214, v214, v150
	v_mul_f32_e32 v215, v215, v150
	v_mul_f32_e32 v200, v200, v151
	v_mul_f32_e32 v201, v201, v151
	v_mul_f32_e32 v216, v216, v151
	v_mul_f32_e32 v217, v217, v151
	v_mul_f32_e32 v202, v202, v152
	v_mul_f32_e32 v203, v203, v152
	v_mul_f32_e32 v218, v218, v152
	v_mul_f32_e32 v219, v219, v152
	v_mul_f32_e32 v204, v204, v153
	v_mul_f32_e32 v205, v205, v153
	v_mul_f32_e32 v220, v220, v153
	v_mul_f32_e32 v221, v221, v153
.Lq_ng_2:
	s_waitcnt lgkmcnt(14)
	v_cvt_pk_bf16_f32 v222, v190, v192
	s_waitcnt lgkmcnt(12)
	v_cvt_pk_bf16_f32 v223, v194, v196
	s_waitcnt lgkmcnt(10)
	v_cvt_pk_bf16_f32 v224, v198, v200
	s_waitcnt lgkmcnt(8)
	v_cvt_pk_bf16_f32 v225, v202, v204
	global_store_dwordx4 v170, v[222:225], s[18:19] nt
	v_cvt_pk_bf16_f32 v226, v191, v193
	v_cvt_pk_bf16_f32 v227, v195, v197
	v_cvt_pk_bf16_f32 v228, v199, v201
	v_cvt_pk_bf16_f32 v229, v203, v205
	global_store_dwordx4 v171, v[226:229], s[18:19] nt
	s_waitcnt lgkmcnt(6)
	v_cvt_pk_bf16_f32 v222, v206, v208
	s_waitcnt lgkmcnt(4)
	v_cvt_pk_bf16_f32 v223, v210, v212
	s_waitcnt lgkmcnt(2)
	v_cvt_pk_bf16_f32 v224, v214, v216
	s_waitcnt lgkmcnt(0)
	v_cvt_pk_bf16_f32 v225, v218, v220
	global_store_dwordx4 v172, v[222:225], s[18:19] nt
	v_cvt_pk_bf16_f32 v226, v207, v209
	v_cvt_pk_bf16_f32 v227, v211, v213
	v_cvt_pk_bf16_f32 v228, v215, v217
	v_cvt_pk_bf16_f32 v229, v219, v221
	global_store_dwordx4 v173, v[226:229], s[18:19] nt
	s_add_u32 s18, s6, 768
	s_addc_u32 s19, s7, 0
	s_nop 1
	global_load_dwordx4 v[66:69], v162, s[18:19] nt
	global_load_dwordx4 v[70:73], v163, s[18:19] nt
	global_load_dwordx4 v[74:77], v164, s[18:19] nt
	global_load_dwordx4 v[78:81], v165, s[18:19] nt
	global_load_dwordx4 v[82:85], v166, s[18:19] nt
	global_load_dwordx4 v[86:89], v167, s[18:19] nt
	global_load_dwordx4 v[90:93], v168, s[18:19] nt
	global_load_dwordx4 v[94:97], v169, s[18:19] nt
	global_load_dwordx4 v[146:149], v178, s[8:9]
	global_load_dwordx4 v[150:153], v178, s[8:9] offset:16
	s_bitcmp1_b32 s13, 0
	s_cselect_b32 s2, 3, 3
	s_mul_i32 s2, s2, s12
	s_add_u32 s18, s10, s2
	s_addc_u32 s19, s11, 0
	s_waitcnt vmcnt(51)
	ds_write2_b32 v180, v98, v99 offset1:1
	ds_write2_b32 v180, v100, v101 offset0:2 offset1:3
	s_waitcnt vmcnt(50)
	ds_write2_b32 v181, v102, v103 offset1:1
	ds_write2_b32 v181, v104, v105 offset0:2 offset1:3
	s_waitcnt vmcnt(49)
	ds_write2_b32 v182, v106, v107 offset1:1
	ds_write2_b32 v182, v108, v109 offset0:2 offset1:3
	s_waitcnt vmcnt(48)
	ds_write2_b32 v183, v110, v111 offset1:1
	ds_write2_b32 v183, v112, v113 offset0:2 offset1:3
	s_waitcnt vmcnt(47)
	ds_write2_b32 v184, v114, v115 offset1:1
	ds_write2_b32 v184, v116, v117 offset0:2 offset1:3
	s_waitcnt vmcnt(46)
	ds_write2_b32 v185, v118, v119 offset1:1
	ds_write2_b32 v185, v120, v121 offset0:2 offset1:3
	s_waitcnt vmcnt(45)
	ds_write2_b32 v186, v122, v123 offset1:1
	ds_write2_b32 v186, v124, v125 offset0:2 offset1:3
	s_waitcnt vmcnt(44)
	ds_write2_b32 v187, v126, v127 offset1:1
	ds_write2_b32 v187, v128, v129 offset0:2 offset1:3
	s_waitcnt lgkmcnt(0)
	ds_read2_b32 v[190:191], v188 offset0:0 offset1:8
	ds_read2_b32 v[192:193], v188 offset0:33 offset1:41
	ds_read2_b32 v[194:195], v188 offset0:66 offset1:74
	ds_read2_b32 v[196:197], v188 offset0:99 offset1:107
	ds_read2_b32 v[198:199], v188 offset0:132 offset1:140
	ds_read2_b32 v[200:201], v188 offset0:165 offset1:173
	ds_read2_b32 v[202:203], v188 offset0:198 offset1:206
	ds_read2_b32 v[204:205], v188 offset0:231 offset1:239
	ds_read2_b32 v[206:207], v188 offset0:16 offset1:24
	ds_read2_b32 v[208:209], v188 offset0:49 offset1:57
	ds_read2_b32 v[210:211], v188 offset0:82 offset1:90
	ds_read2_b32 v[212:213], v188 offset0:115 offset1:123
	ds_read2_b32 v[214:215], v188 offset0:148 offset1:156
	ds_read2_b32 v[216:217], v188 offset0:181 offset1:189
	ds_read2_b32 v[218:219], v188 offset0:214 offset1:222
	ds_read2_b32 v[220:221], v188 offset0:247 offset1:255
	s_bitcmp1_b32 s13, 1
	s_cbranch_scc0 .Lq_ng_3
	s_waitcnt vmcnt(42)
	s_waitcnt lgkmcnt(0)
	v_mul_f32_e32 v190, v190, v154
	v_mul_f32_e32 v191, v191, v154
	v_mul_f32_e32 v206, v206, v154
	v_mul_f32_e32 v207, v207, v154
	v_mul_f32_e32 v192, v192, v155
	v_mul_f32_e32 v193, v193, v155
	v_mul_f32_e32 v208, v208, v155
	v_mul_f32_e32 v209, v209, v155
	v_mul_f32_e32 v194, v194, v156
	v_mul_f32_e32 v195, v195, v156
	v_mul_f32_e32 v210, v210, v156
	v_mul_f32_e32 v211, v211, v156
	v_mul_f32_e32 v196, v196, v157
	v_mul_f32_e32 v197, v197, v157
	v_mul_f32_e32 v212, v212, v157
	v_mul_f32_e32 v213, v213, v157
	v_mul_f32_e32 v198, v198, v158
	v_mul_f32_e32 v199, v199, v158
	v_mul_f32_e32 v214, v214, v158
	v_mul_f32_e32 v215, v215, v158
	v_mul_f32_e32 v200, v200, v159
	v_mul_f32_e32 v201, v201, v159
	v_mul_f32_e32 v216, v216, v159
	v_mul_f32_e32 v217, v217, v159
	v_mul_f32_e32 v202, v202, v160
	v_mul_f32_e32 v203, v203, v160
	v_mul_f32_e32 v218, v218, v160
	v_mul_f32_e32 v219, v219, v160
	v_mul_f32_e32 v204, v204, v161
	v_mul_f32_e32 v205, v205, v161
	v_mul_f32_e32 v220, v220, v161
	v_mul_f32_e32 v221, v221, v161
.Lq_ng_3:
	s_waitcnt lgkmcnt(14)
	v_cvt_pk_bf16_f32 v222, v190, v192
	s_waitcnt lgkmcnt(12)
	v_cvt_pk_bf16_f32 v223, v194, v196
	s_waitcnt lgkmcnt(10)
	v_cvt_pk_bf16_f32 v224, v198, v200
	s_waitcnt lgkmcnt(8)
	v_cvt_pk_bf16_f32 v225, v202, v204
	global_store_dwordx4 v170, v[222:225], s[18:19] nt
	v_cvt_pk_bf16_f32 v226, v191, v193
	v_cvt_pk_bf16_f32 v227, v195, v197
	v_cvt_pk_bf16_f32 v228, v199, v201
	v_cvt_pk_bf16_f32 v229, v203, v205
	global_store_dwordx4 v171, v[226:229], s[18:19] nt
	s_waitcnt lgkmcnt(6)
	v_cvt_pk_bf16_f32 v222, v206, v208
	s_waitcnt lgkmcnt(4)
	v_cvt_pk_bf16_f32 v223, v210, v212
	s_waitcnt lgkmcnt(2)
	v_cvt_pk_bf16_f32 v224, v214, v216
	s_waitcnt lgkmcnt(0)
	v_cvt_pk_bf16_f32 v225, v218, v220
	global_store_dwordx4 v172, v[222:225], s[18:19] nt
	v_cvt_pk_bf16_f32 v226, v207, v209
	v_cvt_pk_bf16_f32 v227, v211, v213
	v_cvt_pk_bf16_f32 v228, v215, v217
	v_cvt_pk_bf16_f32 v229, v219, v221
	global_store_dwordx4 v173, v[226:229], s[18:19] nt
	s_add_u32 s18, s6, 896
	s_addc_u32 s19, s7, 0
	s_nop 1
	global_load_dwordx4 v[98:101], v162, s[18:19] nt
	global_load_dwordx4 v[102:105], v163, s[18:19] nt
	global_load_dwordx4 v[106:109], v164, s[18:19] nt
	global_load_dwordx4 v[110:113], v165, s[18:19] nt
	global_load_dwordx4 v[114:117], v166, s[18:19] nt
	global_load_dwordx4 v[118:121], v167, s[18:19] nt
	global_load_dwordx4 v[122:125], v168, s[18:19] nt
	global_load_dwordx4 v[126:129], v169, s[18:19] nt
	global_load_dwordx4 v[154:157], v178, s[8:9]
	global_load_dwordx4 v[158:161], v178, s[8:9] offset:16
.Lq_loop:
	s_nop 0
	v_readfirstlane_b32 s20, v230
	s_cmp_lt_u32 s20, 0x4e00
	s_cbranch_scc0 .Lq_drain
	s_mov_b64 exec, 1
	global_atomic_add v230, v232, v231, s[28:29] offset:256 sc0
	s_mov_b64 exec, -1
	s_bitcmp1_b32 s13, 0
	s_cselect_b32 s2, 8, 4
	s_mul_i32 s2, s2, s12
	s_add_u32 s18, s10, s2
	s_addc_u32 s19, s11, 0
	s_waitcnt vmcnt(52)
	ds_write2_b32 v180, v2, v3 offset1:1
	ds_write2_b32 v180, v4, v5 offset0:2 offset1:3
	s_waitcnt vmcnt(51)
	ds_write2_b32 v181, v6, v7 offset1:1
	ds_write2_b32 v181, v8, v9 offset0:2 offset1:3
	s_waitcnt vmcnt(50)
	ds_write2_b32 v182, v10, v11 offset1:1
	ds_write2_b32 v182, v12, v13 offset0:2 offset1:3
	s_waitcnt vmcnt(49)
	ds_write2_b32 v183, v14, v15 offset1:1
	ds_write2_b32 v183, v16, v17 offset0:2 offset1:3
	s_waitcnt vmcnt(48)
	ds_write2_b32 v184, v18, v19 offset1:1
	ds_write2_b32 v184, v20, v21 offset0:2 offset1:3
	s_waitcnt vmcnt(47)
	ds_write2_b32 v185, v22, v23 offset1:1
	ds_write2_b32 v185, v24, v25 offset0:2 offset1:3
	s_waitcnt vmcnt(46)
	ds_write2_b32 v186, v26, v27 offset1:1
	ds_write2_b32 v186, v28, v29 offset0:2 offset1:3
	s_waitcnt vmcnt(45)
	ds_write2_b32 v187, v30, v31 offset1:1
	ds_write2_b32 v187, v32, v33 offset0:2 offset1:3
	s_waitcnt lgkmcnt(0)
	ds_read2_b32 v[190:191], v188 offset0:0 offset1:8
	ds_read2_b32 v[192:193], v188 offset0:33 offset1:41
	ds_read2_b32 v[194:195], v188 offset0:66 offset1:74
	ds_read2_b32 v[196:197], v188 offset0:99 offset1:107
	ds_read2_b32 v[198:199], v188 offset0:132 offset1:140
	ds_read2_b32 v[200:201], v188 offset0:165 offset1:173
	ds_read2_b32 v[202:203], v188 offset0:198 offset1:206
	ds_read2_b32 v[204:205], v188 offset0:231 offset1:239
	ds_read2_b32 v[206:207], v188 offset0:16 offset1:24
	ds_read2_b32 v[208:209], v188 offset0:49 offset1:57
	ds_read2_b32 v[210:211], v188 offset0:82 offset1:90
	ds_read2_b32 v[212:213], v188 offset0:115 offset1:123
	ds_read2_b32 v[214:215], v188 offset0:148 offset1:156
	ds_read2_b32 v[216:217], v188 offset0:181 offset1:189
	ds_read2_b32 v[218:219], v188 offset0:214 offset1:222
	ds_read2_b32 v[220:221], v188 offset0:247 offset1:255
	s_bitcmp1_b32 s13, 1
	s_cbranch_scc0 .Lq_ng_4
	s_waitcnt vmcnt(43)
	s_waitcnt lgkmcnt(0)
	v_mul_f32_e32 v190, v190, v130
	v_mul_f32_e32 v191, v191, v130
	v_mul_f32_e32 v206, v206, v130
	v_mul_f32_e32 v207, v207, v130
	v_mul_f32_e32 v192, v192, v131
	v_mul_f32_e32 v193, v193, v131
	v_mul_f32_e32 v208, v208, v131
	v_mul_f32_e32 v209, v209, v131
	v_mul_f32_e32 v194, v194, v132
	v_mul_f32_e32 v195, v195, v132
	v_mul_f32_e32 v210, v210, v132
	v_mul_f32_e32 v211, v211, v132
	v_mul_f32_e32 v196, v196, v133
	v_mul_f32_e32 v197, v197, v133
	v_mul_f32_e32 v212, v212, v133
	v_mul_f32_e32 v213, v213, v133
	v_mul_f32_e32 v198, v198, v134
	v_mul_f32_e32 v199, v199, v134
	v_mul_f32_e32 v214, v214, v134
	v_mul_f32_e32 v215, v215, v134
	v_mul_f32_e32 v200, v200, v135
	v_mul_f32_e32 v201, v201, v135
	v_mul_f32_e32 v216, v216, v135
	v_mul_f32_e32 v217, v217, v135
	v_mul_f32_e32 v202, v202, v136
	v_mul_f32_e32 v203, v203, v136
	v_mul_f32_e32 v218, v218, v136
	v_mul_f32_e32 v219, v219, v136
	v_mul_f32_e32 v204, v204, v137
	v_mul_f32_e32 v205, v205, v137
	v_mul_f32_e32 v220, v220, v137
	v_mul_f32_e32 v221, v221, v137
.Lq_ng_4:
	s_waitcnt lgkmcnt(14)
	v_cvt_pk_bf16_f32 v222, v190, v192
	s_waitcnt lgkmcnt(12)
	v_cvt_pk_bf16_f32 v223, v194, v196
	s_waitcnt lgkmcnt(10)
	v_cvt_pk_bf16_f32 v224, v198, v200
	s_waitcnt lgkmcnt(8)
	v_cvt_pk_bf16_f32 v225, v202, v204
	global_store_dwordx4 v170, v[222:225], s[18:19] nt
	v_cvt_pk_bf16_f32 v226, v191, v193
	v_cvt_pk_bf16_f32 v227, v195, v197
	v_cvt_pk_bf16_f32 v228, v199, v201
	v_cvt_pk_bf16_f32 v229, v203, v205
	global_store_dwordx4 v171, v[226:229], s[18:19] nt
	s_waitcnt lgkmcnt(6)
	v_cvt_pk_bf16_f32 v222, v206, v208
	s_waitcnt lgkmcnt(4)
	v_cvt_pk_bf16_f32 v223, v210, v212
	s_waitcnt lgkmcnt(2)
	v_cvt_pk_bf16_f32 v224, v214, v216
	s_waitcnt lgkmcnt(0)
	v_cvt_pk_bf16_f32 v225, v218, v220
	global_store_dwordx4 v172, v[222:225], s[18:19] nt
	v_cvt_pk_bf16_f32 v226, v207, v209
	v_cvt_pk_bf16_f32 v227, v211, v213
	v_cvt_pk_bf16_f32 v228, v215, v217
	v_cvt_pk_bf16_f32 v229, v219, v221
	global_store_dwordx4 v173, v[226:229], s[18:19] nt
	s_lshl_b32 s21, s20, 3
	s_mov_b32 s17, 0
	v_readlane_b32 s8, v254, 12
	v_readlane_b32 s9, v254, 13
	s_mov_b32 s59, 0
	s_mov_b32 s58, 0
	s_cmp_lt_u32 s21, 0x1000
	s_cbranch_scc0 .Lq_l_n1
	s_lshr_b32 s22, s21, 6
	s_and_b32 s23, s21, 63
	s_mov_b32 s52, 0x800
	s_mov_b32 s53, 0x1000
	s_mov_b64 s[54:55], s[82:83]
	v_readlane_b32 s56, v254, 28
	v_readlane_b32 s57, v254, 29
	s_lshl_b32 s18, s23, 5
	s_branch .Lq_l_common

.Lq_l_common:
	s_lshl_b32 s2, s52, 8
	s_mul_i32 s3, s22, s2
	s_lshl_b32 s2, s23, 7
	s_add_u32 s3, s3, s2
	s_add_u32 s6, s54, s3
	s_addc_u32 s7, s55, 0
	s_lshl_b32 s2, s53, 1
	s_mul_i32 s3, s18, s2
	s_lshl_b32 s2, s22, 7
	s_add_u32 s3, s3, s2
	s_add_u32 s14, s56, s3
	s_addc_u32 s15, s57, 0
	s_lshl_b32 s16, s53, 6
	s_mul_i32 s2, s22, s59
	s_lshl_b32 s2, s2, 8
	s_add_u32 s8, s8, s2
	s_addc_u32 s9, s9, 0
	s_lshl_b32 s2, s52, 2
	v_mul_u32_u24_e32 v235, s2, v233
	v_add_u32_e32 v162, v235, v234
	s_lshl_b32 s2, s52, 5
	v_add_u32_e32 v163, s2, v162
	v_add_u32_e32 v164, s2, v163
	v_add_u32_e32 v165, s2, v164
	v_add_u32_e32 v166, s2, v165
	v_add_u32_e32 v167, s2, v166
	v_add_u32_e32 v168, s2, v167
	v_add_u32_e32 v169, s2, v168
	s_lshl_b32 s2, s53, 1
	v_mul_u32_u24_e32 v235, s2, v233
	v_add_u32_e32 v174, v235, v234
	s_lshl_b32 s2, s53, 4
	v_add_u32_e32 v175, s2, v174
	v_add_u32_e32 v176, s2, v175
	v_add_u32_e32 v177, s2, v176
	s_mov_b64 s[18:19], s[6:7]
	s_nop 1
	global_load_dwordx4 v[2:5], v162, s[18:19] nt
	global_load_dwordx4 v[6:9], v163, s[18:19] nt
	global_load_dwordx4 v[10:13], v164, s[18:19] nt
	global_load_dwordx4 v[14:17], v165, s[18:19] nt
	global_load_dwordx4 v[18:21], v166, s[18:19] nt
	global_load_dwordx4 v[22:25], v167, s[18:19] nt
	global_load_dwordx4 v[26:29], v168, s[18:19] nt
	global_load_dwordx4 v[30:33], v169, s[18:19] nt
	global_load_dwordx4 v[130:133], v178, s[8:9]
	global_load_dwordx4 v[134:137], v178, s[8:9] offset:16
	s_bitcmp1_b32 s13, 0
	s_cselect_b32 s2, 9, 5
	s_mul_i32 s2, s2, s12
	s_add_u32 s18, s10, s2
	s_addc_u32 s19, s11, 0
	s_waitcnt vmcnt(52)
	ds_write2_b32 v180, v34, v35 offset1:1
	ds_write2_b32 v180, v36, v37 offset0:2 offset1:3
	s_waitcnt vmcnt(51)
	ds_write2_b32 v181, v38, v39 offset1:1
	ds_write2_b32 v181, v40, v41 offset0:2 offset1:3
	s_waitcnt vmcnt(50)
	ds_write2_b32 v182, v42, v43 offset1:1
	ds_write2_b32 v182, v44, v45 offset0:2 offset1:3
	s_waitcnt vmcnt(49)
	ds_write2_b32 v183, v46, v47 offset1:1
	ds_write2_b32 v183, v48, v49 offset0:2 offset1:3
	s_waitcnt vmcnt(48)
	ds_write2_b32 v184, v50, v51 offset1:1
	ds_write2_b32 v184, v52, v53 offset0:2 offset1:3
	s_waitcnt vmcnt(47)
	ds_write2_b32 v185, v54, v55 offset1:1
	ds_write2_b32 v185, v56, v57 offset0:2 offset1:3
	s_waitcnt vmcnt(46)
	ds_write2_b32 v186, v58, v59 offset1:1
	ds_write2_b32 v186, v60, v61 offset0:2 offset1:3
	s_waitcnt vmcnt(45)
	ds_write2_b32 v187, v62, v63 offset1:1
	ds_write2_b32 v187, v64, v65 offset0:2 offset1:3
	s_waitcnt lgkmcnt(0)
	ds_read2_b32 v[190:191], v188 offset0:0 offset1:8
	ds_read2_b32 v[192:193], v188 offset0:33 offset1:41
	ds_read2_b32 v[194:195], v188 offset0:66 offset1:74
	ds_read2_b32 v[196:197], v188 offset0:99 offset1:107
	ds_read2_b32 v[198:199], v188 offset0:132 offset1:140
	ds_read2_b32 v[200:201], v188 offset0:165 offset1:173
	ds_read2_b32 v[202:203], v188 offset0:198 offset1:206
	ds_read2_b32 v[204:205], v188 offset0:231 offset1:239
	ds_read2_b32 v[206:207], v188 offset0:16 offset1:24
	ds_read2_b32 v[208:209], v188 offset0:49 offset1:57
	ds_read2_b32 v[210:211], v188 offset0:82 offset1:90
	ds_read2_b32 v[212:213], v188 offset0:115 offset1:123
	ds_read2_b32 v[214:215], v188 offset0:148 offset1:156
	ds_read2_b32 v[216:217], v188 offset0:181 offset1:189
	ds_read2_b32 v[218:219], v188 offset0:214 offset1:222
	ds_read2_b32 v[220:221], v188 offset0:247 offset1:255
	s_bitcmp1_b32 s13, 1
	s_cbranch_scc0 .Lq_ng_5
	s_waitcnt vmcnt(43)
	s_waitcnt lgkmcnt(0)
	v_mul_f32_e32 v190, v190, v138
	v_mul_f32_e32 v191, v191, v138
	v_mul_f32_e32 v206, v206, v138
	v_mul_f32_e32 v207, v207, v138
	v_mul_f32_e32 v192, v192, v139
	v_mul_f32_e32 v193, v193, v139
	v_mul_f32_e32 v208, v208, v139
	v_mul_f32_e32 v209, v209, v139
	v_mul_f32_e32 v194, v194, v140
	v_mul_f32_e32 v195, v195, v140
	v_mul_f32_e32 v210, v210, v140
	v_mul_f32_e32 v211, v211, v140
	v_mul_f32_e32 v196, v196, v141
	v_mul_f32_e32 v197, v197, v141
	v_mul_f32_e32 v212, v212, v141
	v_mul_f32_e32 v213, v213, v141
	v_mul_f32_e32 v198, v198, v142
	v_mul_f32_e32 v199, v199, v142
	v_mul_f32_e32 v214, v214, v142
	v_mul_f32_e32 v215, v215, v142
	v_mul_f32_e32 v200, v200, v143
	v_mul_f32_e32 v201, v201, v143
	v_mul_f32_e32 v216, v216, v143
	v_mul_f32_e32 v217, v217, v143
	v_mul_f32_e32 v202, v202, v144
	v_mul_f32_e32 v203, v203, v144
	v_mul_f32_e32 v218, v218, v144
	v_mul_f32_e32 v219, v219, v144
	v_mul_f32_e32 v204, v204, v145
	v_mul_f32_e32 v205, v205, v145
	v_mul_f32_e32 v220, v220, v145
	v_mul_f32_e32 v221, v221, v145
.Lq_ng_5:
	s_waitcnt lgkmcnt(14)
	v_cvt_pk_bf16_f32 v222, v190, v192
	s_waitcnt lgkmcnt(12)
	v_cvt_pk_bf16_f32 v223, v194, v196
	s_waitcnt lgkmcnt(10)
	v_cvt_pk_bf16_f32 v224, v198, v200
	s_waitcnt lgkmcnt(8)
	v_cvt_pk_bf16_f32 v225, v202, v204
	global_store_dwordx4 v170, v[222:225], s[18:19] nt
	v_cvt_pk_bf16_f32 v226, v191, v193
	v_cvt_pk_bf16_f32 v227, v195, v197
	v_cvt_pk_bf16_f32 v228, v199, v201
	v_cvt_pk_bf16_f32 v229, v203, v205
	global_store_dwordx4 v171, v[226:229], s[18:19] nt
	s_waitcnt lgkmcnt(6)
	v_cvt_pk_bf16_f32 v222, v206, v208
	s_waitcnt lgkmcnt(4)
	v_cvt_pk_bf16_f32 v223, v210, v212
	s_waitcnt lgkmcnt(2)
	v_cvt_pk_bf16_f32 v224, v214, v216
	s_waitcnt lgkmcnt(0)
	v_cvt_pk_bf16_f32 v225, v218, v220
	global_store_dwordx4 v172, v[222:225], s[18:19] nt
	v_cvt_pk_bf16_f32 v226, v207, v209
	v_cvt_pk_bf16_f32 v227, v211, v213
	v_cvt_pk_bf16_f32 v228, v215, v217
	v_cvt_pk_bf16_f32 v229, v219, v221
	global_store_dwordx4 v173, v[226:229], s[18:19] nt
	s_add_u32 s18, s6, 128
	s_addc_u32 s19, s7, 0
	s_nop 1
	global_load_dwordx4 v[34:37], v162, s[18:19] nt
	global_load_dwordx4 v[38:41], v163, s[18:19] nt
	global_load_dwordx4 v[42:45], v164, s[18:19] nt
	global_load_dwordx4 v[46:49], v165, s[18:19] nt
	global_load_dwordx4 v[50:53], v166, s[18:19] nt
	global_load_dwordx4 v[54:57], v167, s[18:19] nt
	global_load_dwordx4 v[58:61], v168, s[18:19] nt
	global_load_dwordx4 v[62:65], v169, s[18:19] nt
	global_load_dwordx4 v[138:141], v178, s[8:9]
	global_load_dwordx4 v[142:145], v178, s[8:9] offset:16
	s_bitcmp1_b32 s13, 0
	s_cselect_b32 s2, 10, 6
	s_mul_i32 s2, s2, s12
	s_add_u32 s18, s10, s2
	s_addc_u32 s19, s11, 0
	s_waitcnt vmcnt(52)
	ds_write2_b32 v180, v66, v67 offset1:1
	ds_write2_b32 v180, v68, v69 offset0:2 offset1:3
	s_waitcnt vmcnt(51)
	ds_write2_b32 v181, v70, v71 offset1:1
	ds_write2_b32 v181, v72, v73 offset0:2 offset1:3
	s_waitcnt vmcnt(50)
	ds_write2_b32 v182, v74, v75 offset1:1
	ds_write2_b32 v182, v76, v77 offset0:2 offset1:3
	s_waitcnt vmcnt(49)
	ds_write2_b32 v183, v78, v79 offset1:1
	ds_write2_b32 v183, v80, v81 offset0:2 offset1:3
	s_waitcnt vmcnt(48)
	ds_write2_b32 v184, v82, v83 offset1:1
	ds_write2_b32 v184, v84, v85 offset0:2 offset1:3
	s_waitcnt vmcnt(47)
	ds_write2_b32 v185, v86, v87 offset1:1
	ds_write2_b32 v185, v88, v89 offset0:2 offset1:3
	s_waitcnt vmcnt(46)
	ds_write2_b32 v186, v90, v91 offset1:1
	ds_write2_b32 v186, v92, v93 offset0:2 offset1:3
	s_waitcnt vmcnt(45)
	ds_write2_b32 v187, v94, v95 offset1:1
	ds_write2_b32 v187, v96, v97 offset0:2 offset1:3
	s_waitcnt lgkmcnt(0)
	ds_read2_b32 v[190:191], v188 offset0:0 offset1:8
	ds_read2_b32 v[192:193], v188 offset0:33 offset1:41
	ds_read2_b32 v[194:195], v188 offset0:66 offset1:74
	ds_read2_b32 v[196:197], v188 offset0:99 offset1:107
	ds_read2_b32 v[198:199], v188 offset0:132 offset1:140
	ds_read2_b32 v[200:201], v188 offset0:165 offset1:173
	ds_read2_b32 v[202:203], v188 offset0:198 offset1:206
	ds_read2_b32 v[204:205], v188 offset0:231 offset1:239
	ds_read2_b32 v[206:207], v188 offset0:16 offset1:24
	ds_read2_b32 v[208:209], v188 offset0:49 offset1:57
	ds_read2_b32 v[210:211], v188 offset0:82 offset1:90
	ds_read2_b32 v[212:213], v188 offset0:115 offset1:123
	ds_read2_b32 v[214:215], v188 offset0:148 offset1:156
	ds_read2_b32 v[216:217], v188 offset0:181 offset1:189
	ds_read2_b32 v[218:219], v188 offset0:214 offset1:222
	ds_read2_b32 v[220:221], v188 offset0:247 offset1:255
	s_bitcmp1_b32 s13, 1
	s_cbranch_scc0 .Lq_ng_6
	s_waitcnt vmcnt(43)
	s_waitcnt lgkmcnt(0)
	v_mul_f32_e32 v190, v190, v146
	v_mul_f32_e32 v191, v191, v146
	v_mul_f32_e32 v206, v206, v146
	v_mul_f32_e32 v207, v207, v146
	v_mul_f32_e32 v192, v192, v147
	v_mul_f32_e32 v193, v193, v147
	v_mul_f32_e32 v208, v208, v147
	v_mul_f32_e32 v209, v209, v147
	v_mul_f32_e32 v194, v194, v148
	v_mul_f32_e32 v195, v195, v148
	v_mul_f32_e32 v210, v210, v148
	v_mul_f32_e32 v211, v211, v148
	v_mul_f32_e32 v196, v196, v149
	v_mul_f32_e32 v197, v197, v149
	v_mul_f32_e32 v212, v212, v149
	v_mul_f32_e32 v213, v213, v149
	v_mul_f32_e32 v198, v198, v150
	v_mul_f32_e32 v199, v199, v150
	v_mul_f32_e32 v214, v214, v150
	v_mul_f32_e32 v215, v215, v150
	v_mul_f32_e32 v200, v200, v151
	v_mul_f32_e32 v201, v201, v151
	v_mul_f32_e32 v216, v216, v151
	v_mul_f32_e32 v217, v217, v151
	v_mul_f32_e32 v202, v202, v152
	v_mul_f32_e32 v203, v203, v152
	v_mul_f32_e32 v218, v218, v152
	v_mul_f32_e32 v219, v219, v152
	v_mul_f32_e32 v204, v204, v153
	v_mul_f32_e32 v205, v205, v153
	v_mul_f32_e32 v220, v220, v153
	v_mul_f32_e32 v221, v221, v153
.Lq_ng_6:
	s_waitcnt lgkmcnt(14)
	v_cvt_pk_bf16_f32 v222, v190, v192
	s_waitcnt lgkmcnt(12)
	v_cvt_pk_bf16_f32 v223, v194, v196
	s_waitcnt lgkmcnt(10)
	v_cvt_pk_bf16_f32 v224, v198, v200
	s_waitcnt lgkmcnt(8)
	v_cvt_pk_bf16_f32 v225, v202, v204
	global_store_dwordx4 v170, v[222:225], s[18:19] nt
	v_cvt_pk_bf16_f32 v226, v191, v193
	v_cvt_pk_bf16_f32 v227, v195, v197
	v_cvt_pk_bf16_f32 v228, v199, v201
	v_cvt_pk_bf16_f32 v229, v203, v205
	global_store_dwordx4 v171, v[226:229], s[18:19] nt
	s_waitcnt lgkmcnt(6)
	v_cvt_pk_bf16_f32 v222, v206, v208
	s_waitcnt lgkmcnt(4)
	v_cvt_pk_bf16_f32 v223, v210, v212
	s_waitcnt lgkmcnt(2)
	v_cvt_pk_bf16_f32 v224, v214, v216
	s_waitcnt lgkmcnt(0)
	v_cvt_pk_bf16_f32 v225, v218, v220
	global_store_dwordx4 v172, v[222:225], s[18:19] nt
	v_cvt_pk_bf16_f32 v226, v207, v209
	v_cvt_pk_bf16_f32 v227, v211, v213
	v_cvt_pk_bf16_f32 v228, v215, v217
	v_cvt_pk_bf16_f32 v229, v219, v221
	global_store_dwordx4 v173, v[226:229], s[18:19] nt
	s_add_u32 s18, s6, 256
	s_addc_u32 s19, s7, 0
	s_nop 1
	global_load_dwordx4 v[66:69], v162, s[18:19] nt
	global_load_dwordx4 v[70:73], v163, s[18:19] nt
	global_load_dwordx4 v[74:77], v164, s[18:19] nt
	global_load_dwordx4 v[78:81], v165, s[18:19] nt
	global_load_dwordx4 v[82:85], v166, s[18:19] nt
	global_load_dwordx4 v[86:89], v167, s[18:19] nt
	global_load_dwordx4 v[90:93], v168, s[18:19] nt
	global_load_dwordx4 v[94:97], v169, s[18:19] nt
	global_load_dwordx4 v[146:149], v178, s[8:9]
	global_load_dwordx4 v[150:153], v178, s[8:9] offset:16
	s_bitcmp1_b32 s13, 0
	s_cselect_b32 s2, 11, 7
	s_mul_i32 s2, s2, s12
	s_add_u32 s18, s10, s2
	s_addc_u32 s19, s11, 0
	s_waitcnt vmcnt(52)
	ds_write2_b32 v180, v98, v99 offset1:1
	ds_write2_b32 v180, v100, v101 offset0:2 offset1:3
	s_waitcnt vmcnt(51)
	ds_write2_b32 v181, v102, v103 offset1:1
	ds_write2_b32 v181, v104, v105 offset0:2 offset1:3
	s_waitcnt vmcnt(50)
	ds_write2_b32 v182, v106, v107 offset1:1
	ds_write2_b32 v182, v108, v109 offset0:2 offset1:3
	s_waitcnt vmcnt(49)
	ds_write2_b32 v183, v110, v111 offset1:1
	ds_write2_b32 v183, v112, v113 offset0:2 offset1:3
	s_waitcnt vmcnt(48)
	ds_write2_b32 v184, v114, v115 offset1:1
	ds_write2_b32 v184, v116, v117 offset0:2 offset1:3
	s_waitcnt vmcnt(47)
	ds_write2_b32 v185, v118, v119 offset1:1
	ds_write2_b32 v185, v120, v121 offset0:2 offset1:3
	s_waitcnt vmcnt(46)
	ds_write2_b32 v186, v122, v123 offset1:1
	ds_write2_b32 v186, v124, v125 offset0:2 offset1:3
	s_waitcnt vmcnt(45)
	ds_write2_b32 v187, v126, v127 offset1:1
	ds_write2_b32 v187, v128, v129 offset0:2 offset1:3
	s_waitcnt lgkmcnt(0)
	ds_read2_b32 v[190:191], v188 offset0:0 offset1:8
	ds_read2_b32 v[192:193], v188 offset0:33 offset1:41
	ds_read2_b32 v[194:195], v188 offset0:66 offset1:74
	ds_read2_b32 v[196:197], v188 offset0:99 offset1:107
	ds_read2_b32 v[198:199], v188 offset0:132 offset1:140
	ds_read2_b32 v[200:201], v188 offset0:165 offset1:173
	ds_read2_b32 v[202:203], v188 offset0:198 offset1:206
	ds_read2_b32 v[204:205], v188 offset0:231 offset1:239
	ds_read2_b32 v[206:207], v188 offset0:16 offset1:24
	ds_read2_b32 v[208:209], v188 offset0:49 offset1:57
	ds_read2_b32 v[210:211], v188 offset0:82 offset1:90
	ds_read2_b32 v[212:213], v188 offset0:115 offset1:123
	ds_read2_b32 v[214:215], v188 offset0:148 offset1:156
	ds_read2_b32 v[216:217], v188 offset0:181 offset1:189
	ds_read2_b32 v[218:219], v188 offset0:214 offset1:222
	ds_read2_b32 v[220:221], v188 offset0:247 offset1:255
	s_bitcmp1_b32 s13, 1
	s_cbranch_scc0 .Lq_ng_7
	s_waitcnt vmcnt(43)
	s_waitcnt lgkmcnt(0)
	v_mul_f32_e32 v190, v190, v154
	v_mul_f32_e32 v191, v191, v154
	v_mul_f32_e32 v206, v206, v154
	v_mul_f32_e32 v207, v207, v154
	v_mul_f32_e32 v192, v192, v155
	v_mul_f32_e32 v193, v193, v155
	v_mul_f32_e32 v208, v208, v155
	v_mul_f32_e32 v209, v209, v155
	v_mul_f32_e32 v194, v194, v156
	v_mul_f32_e32 v195, v195, v156
	v_mul_f32_e32 v210, v210, v156
	v_mul_f32_e32 v211, v211, v156
	v_mul_f32_e32 v196, v196, v157
	v_mul_f32_e32 v197, v197, v157
	v_mul_f32_e32 v212, v212, v157
	v_mul_f32_e32 v213, v213, v157
	v_mul_f32_e32 v198, v198, v158
	v_mul_f32_e32 v199, v199, v158
	v_mul_f32_e32 v214, v214, v158
	v_mul_f32_e32 v215, v215, v158
	v_mul_f32_e32 v200, v200, v159
	v_mul_f32_e32 v201, v201, v159
	v_mul_f32_e32 v216, v216, v159
	v_mul_f32_e32 v217, v217, v159
	v_mul_f32_e32 v202, v202, v160
	v_mul_f32_e32 v203, v203, v160
	v_mul_f32_e32 v218, v218, v160
	v_mul_f32_e32 v219, v219, v160
	v_mul_f32_e32 v204, v204, v161
	v_mul_f32_e32 v205, v205, v161
	v_mul_f32_e32 v220, v220, v161
	v_mul_f32_e32 v221, v221, v161
.Lq_ng_7:
	s_waitcnt lgkmcnt(14)
	v_cvt_pk_bf16_f32 v222, v190, v192
	s_waitcnt lgkmcnt(12)
	v_cvt_pk_bf16_f32 v223, v194, v196
	s_waitcnt lgkmcnt(10)
	v_cvt_pk_bf16_f32 v224, v198, v200
	s_waitcnt lgkmcnt(8)
	v_cvt_pk_bf16_f32 v225, v202, v204
	global_store_dwordx4 v170, v[222:225], s[18:19] nt
	v_cvt_pk_bf16_f32 v226, v191, v193
	v_cvt_pk_bf16_f32 v227, v195, v197
	v_cvt_pk_bf16_f32 v228, v199, v201
	v_cvt_pk_bf16_f32 v229, v203, v205
	global_store_dwordx4 v171, v[226:229], s[18:19] nt
	s_waitcnt lgkmcnt(6)
	v_cvt_pk_bf16_f32 v222, v206, v208
	s_waitcnt lgkmcnt(4)
	v_cvt_pk_bf16_f32 v223, v210, v212
	s_waitcnt lgkmcnt(2)
	v_cvt_pk_bf16_f32 v224, v214, v216
	s_waitcnt lgkmcnt(0)
	v_cvt_pk_bf16_f32 v225, v218, v220
	global_store_dwordx4 v172, v[222:225], s[18:19] nt
	v_cvt_pk_bf16_f32 v226, v207, v209
	v_cvt_pk_bf16_f32 v227, v211, v213
	v_cvt_pk_bf16_f32 v228, v215, v217
	v_cvt_pk_bf16_f32 v229, v219, v221
	global_store_dwordx4 v173, v[226:229], s[18:19] nt
	s_add_u32 s18, s6, 384
	s_addc_u32 s19, s7, 0
	s_nop 1
	global_load_dwordx4 v[98:101], v162, s[18:19] nt
	global_load_dwordx4 v[102:105], v163, s[18:19] nt
	global_load_dwordx4 v[106:109], v164, s[18:19] nt
	global_load_dwordx4 v[110:113], v165, s[18:19] nt
	global_load_dwordx4 v[114:117], v166, s[18:19] nt
	global_load_dwordx4 v[118:121], v167, s[18:19] nt
	global_load_dwordx4 v[122:125], v168, s[18:19] nt
	global_load_dwordx4 v[126:129], v169, s[18:19] nt
	global_load_dwordx4 v[154:157], v178, s[8:9]
	global_load_dwordx4 v[158:161], v178, s[8:9] offset:16
	s_mov_b64 s[10:11], s[14:15]
	s_mov_b32 s12, s16
	s_mov_b32 s13, s17
	v_mov_b32_e32 v170, v174
	v_mov_b32_e32 v171, v175
	v_mov_b32_e32 v172, v176
	v_mov_b32_e32 v173, v177
	s_bitcmp1_b32 s13, 0
	s_cselect_b32 s2, 0, 0
	s_mul_i32 s2, s2, s12
	s_add_u32 s18, s10, s2
	s_addc_u32 s19, s11, 0
	s_waitcnt vmcnt(51)
	ds_write2_b32 v180, v2, v3 offset1:1
	ds_write2_b32 v180, v4, v5 offset0:2 offset1:3
	s_waitcnt vmcnt(50)
	ds_write2_b32 v181, v6, v7 offset1:1
	ds_write2_b32 v181, v8, v9 offset0:2 offset1:3
	s_waitcnt vmcnt(49)
	ds_write2_b32 v182, v10, v11 offset1:1
	ds_write2_b32 v182, v12, v13 offset0:2 offset1:3
	s_waitcnt vmcnt(48)
	ds_write2_b32 v183, v14, v15 offset1:1
	ds_write2_b32 v183, v16, v17 offset0:2 offset1:3
	s_waitcnt vmcnt(47)
	ds_write2_b32 v184, v18, v19 offset1:1
	ds_write2_b32 v184, v20, v21 offset0:2 offset1:3
	s_waitcnt vmcnt(46)
	ds_write2_b32 v185, v22, v23 offset1:1
	ds_write2_b32 v185, v24, v25 offset0:2 offset1:3
	s_waitcnt vmcnt(45)
	ds_write2_b32 v186, v26, v27 offset1:1
	ds_write2_b32 v186, v28, v29 offset0:2 offset1:3
	s_waitcnt vmcnt(44)
	ds_write2_b32 v187, v30, v31 offset1:1
	ds_write2_b32 v187, v32, v33 offset0:2 offset1:3
	s_waitcnt lgkmcnt(0)
	ds_read2_b32 v[190:191], v188 offset0:0 offset1:8
	ds_read2_b32 v[192:193], v188 offset0:33 offset1:41
	ds_read2_b32 v[194:195], v188 offset0:66 offset1:74
	ds_read2_b32 v[196:197], v188 offset0:99 offset1:107
	ds_read2_b32 v[198:199], v188 offset0:132 offset1:140
	ds_read2_b32 v[200:201], v188 offset0:165 offset1:173
	ds_read2_b32 v[202:203], v188 offset0:198 offset1:206
	ds_read2_b32 v[204:205], v188 offset0:231 offset1:239
	ds_read2_b32 v[206:207], v188 offset0:16 offset1:24
	ds_read2_b32 v[208:209], v188 offset0:49 offset1:57
	ds_read2_b32 v[210:211], v188 offset0:82 offset1:90
	ds_read2_b32 v[212:213], v188 offset0:115 offset1:123
	ds_read2_b32 v[214:215], v188 offset0:148 offset1:156
	ds_read2_b32 v[216:217], v188 offset0:181 offset1:189
	ds_read2_b32 v[218:219], v188 offset0:214 offset1:222
	ds_read2_b32 v[220:221], v188 offset0:247 offset1:255
	s_bitcmp1_b32 s13, 1
	s_cbranch_scc0 .Lq_ng_8
	s_waitcnt vmcnt(42)
	s_waitcnt lgkmcnt(0)
	v_mul_f32_e32 v190, v190, v130
	v_mul_f32_e32 v191, v191, v130
	v_mul_f32_e32 v206, v206, v130
	v_mul_f32_e32 v207, v207, v130
	v_mul_f32_e32 v192, v192, v131
	v_mul_f32_e32 v193, v193, v131
	v_mul_f32_e32 v208, v208, v131
	v_mul_f32_e32 v209, v209, v131
	v_mul_f32_e32 v194, v194, v132
	v_mul_f32_e32 v195, v195, v132
	v_mul_f32_e32 v210, v210, v132
	v_mul_f32_e32 v211, v211, v132
	v_mul_f32_e32 v196, v196, v133
	v_mul_f32_e32 v197, v197, v133
	v_mul_f32_e32 v212, v212, v133
	v_mul_f32_e32 v213, v213, v133
	v_mul_f32_e32 v198, v198, v134
	v_mul_f32_e32 v199, v199, v134
	v_mul_f32_e32 v214, v214, v134
	v_mul_f32_e32 v215, v215, v134
	v_mul_f32_e32 v200, v200, v135
	v_mul_f32_e32 v201, v201, v135
	v_mul_f32_e32 v216, v216, v135
	v_mul_f32_e32 v217, v217, v135
	v_mul_f32_e32 v202, v202, v136
	v_mul_f32_e32 v203, v203, v136
	v_mul_f32_e32 v218, v218, v136
	v_mul_f32_e32 v219, v219, v136
	v_mul_f32_e32 v204, v204, v137
	v_mul_f32_e32 v205, v205, v137
	v_mul_f32_e32 v220, v220, v137
	v_mul_f32_e32 v221, v221, v137
.Lq_ng_8:
	s_waitcnt lgkmcnt(14)
	v_cvt_pk_bf16_f32 v222, v190, v192
	s_waitcnt lgkmcnt(12)
	v_cvt_pk_bf16_f32 v223, v194, v196
	s_waitcnt lgkmcnt(10)
	v_cvt_pk_bf16_f32 v224, v198, v200
	s_waitcnt lgkmcnt(8)
	v_cvt_pk_bf16_f32 v225, v202, v204
	global_store_dwordx4 v170, v[222:225], s[18:19] nt
	v_cvt_pk_bf16_f32 v226, v191, v193
	v_cvt_pk_bf16_f32 v227, v195, v197
	v_cvt_pk_bf16_f32 v228, v199, v201
	v_cvt_pk_bf16_f32 v229, v203, v205
	global_store_dwordx4 v171, v[226:229], s[18:19] nt
	s_waitcnt lgkmcnt(6)
	v_cvt_pk_bf16_f32 v222, v206, v208
	s_waitcnt lgkmcnt(4)
	v_cvt_pk_bf16_f32 v223, v210, v212
	s_waitcnt lgkmcnt(2)
	v_cvt_pk_bf16_f32 v224, v214, v216
	s_waitcnt lgkmcnt(0)
	v_cvt_pk_bf16_f32 v225, v218, v220
	global_store_dwordx4 v172, v[222:225], s[18:19] nt
	v_cvt_pk_bf16_f32 v226, v207, v209
	v_cvt_pk_bf16_f32 v227, v211, v213
	v_cvt_pk_bf16_f32 v228, v215, v217
	v_cvt_pk_bf16_f32 v229, v219, v221
	global_store_dwordx4 v173, v[226:229], s[18:19] nt
	s_add_u32 s18, s6, 512
	s_addc_u32 s19, s7, 0
	s_nop 1
	global_load_dwordx4 v[2:5], v162, s[18:19] nt
	global_load_dwordx4 v[6:9], v163, s[18:19] nt
	global_load_dwordx4 v[10:13], v164, s[18:19] nt
	global_load_dwordx4 v[14:17], v165, s[18:19] nt
	global_load_dwordx4 v[18:21], v166, s[18:19] nt
	global_load_dwordx4 v[22:25], v167, s[18:19] nt
	global_load_dwordx4 v[26:29], v168, s[18:19] nt
	global_load_dwordx4 v[30:33], v169, s[18:19] nt
	global_load_dwordx4 v[130:133], v178, s[8:9]
	global_load_dwordx4 v[134:137], v178, s[8:9] offset:16
	s_bitcmp1_b32 s13, 0
	s_cselect_b32 s2, 1, 1
	s_mul_i32 s2, s2, s12
	s_add_u32 s18, s10, s2
	s_addc_u32 s19, s11, 0
	s_waitcnt vmcnt(51)
	ds_write2_b32 v180, v34, v35 offset1:1
	ds_write2_b32 v180, v36, v37 offset0:2 offset1:3
	s_waitcnt vmcnt(50)
	ds_write2_b32 v181, v38, v39 offset1:1
	ds_write2_b32 v181, v40, v41 offset0:2 offset1:3
	s_waitcnt vmcnt(49)
	ds_write2_b32 v182, v42, v43 offset1:1
	ds_write2_b32 v182, v44, v45 offset0:2 offset1:3
	s_waitcnt vmcnt(48)
	ds_write2_b32 v183, v46, v47 offset1:1
	ds_write2_b32 v183, v48, v49 offset0:2 offset1:3
	s_waitcnt vmcnt(47)
	ds_write2_b32 v184, v50, v51 offset1:1
	ds_write2_b32 v184, v52, v53 offset0:2 offset1:3
	s_waitcnt vmcnt(46)
	ds_write2_b32 v185, v54, v55 offset1:1
	ds_write2_b32 v185, v56, v57 offset0:2 offset1:3
	s_waitcnt vmcnt(45)
	ds_write2_b32 v186, v58, v59 offset1:1
	ds_write2_b32 v186, v60, v61 offset0:2 offset1:3
	s_waitcnt vmcnt(44)
	ds_write2_b32 v187, v62, v63 offset1:1
	ds_write2_b32 v187, v64, v65 offset0:2 offset1:3
	s_waitcnt lgkmcnt(0)
	ds_read2_b32 v[190:191], v188 offset0:0 offset1:8
	ds_read2_b32 v[192:193], v188 offset0:33 offset1:41
	ds_read2_b32 v[194:195], v188 offset0:66 offset1:74
	ds_read2_b32 v[196:197], v188 offset0:99 offset1:107
	ds_read2_b32 v[198:199], v188 offset0:132 offset1:140
	ds_read2_b32 v[200:201], v188 offset0:165 offset1:173
	ds_read2_b32 v[202:203], v188 offset0:198 offset1:206
	ds_read2_b32 v[204:205], v188 offset0:231 offset1:239
	ds_read2_b32 v[206:207], v188 offset0:16 offset1:24
	ds_read2_b32 v[208:209], v188 offset0:49 offset1:57
	ds_read2_b32 v[210:211], v188 offset0:82 offset1:90
	ds_read2_b32 v[212:213], v188 offset0:115 offset1:123
	ds_read2_b32 v[214:215], v188 offset0:148 offset1:156
	ds_read2_b32 v[216:217], v188 offset0:181 offset1:189
	ds_read2_b32 v[218:219], v188 offset0:214 offset1:222
	ds_read2_b32 v[220:221], v188 offset0:247 offset1:255
	s_bitcmp1_b32 s13, 1
	s_cbranch_scc0 .Lq_ng_9
	s_waitcnt vmcnt(42)
	s_waitcnt lgkmcnt(0)
	v_mul_f32_e32 v190, v190, v138
	v_mul_f32_e32 v191, v191, v138
	v_mul_f32_e32 v206, v206, v138
	v_mul_f32_e32 v207, v207, v138
	v_mul_f32_e32 v192, v192, v139
	v_mul_f32_e32 v193, v193, v139
	v_mul_f32_e32 v208, v208, v139
	v_mul_f32_e32 v209, v209, v139
	v_mul_f32_e32 v194, v194, v140
	v_mul_f32_e32 v195, v195, v140
	v_mul_f32_e32 v210, v210, v140
	v_mul_f32_e32 v211, v211, v140
	v_mul_f32_e32 v196, v196, v141
	v_mul_f32_e32 v197, v197, v141
	v_mul_f32_e32 v212, v212, v141
	v_mul_f32_e32 v213, v213, v141
	v_mul_f32_e32 v198, v198, v142
	v_mul_f32_e32 v199, v199, v142
	v_mul_f32_e32 v214, v214, v142
	v_mul_f32_e32 v215, v215, v142
	v_mul_f32_e32 v200, v200, v143
	v_mul_f32_e32 v201, v201, v143
	v_mul_f32_e32 v216, v216, v143
	v_mul_f32_e32 v217, v217, v143
	v_mul_f32_e32 v202, v202, v144
	v_mul_f32_e32 v203, v203, v144
	v_mul_f32_e32 v218, v218, v144
	v_mul_f32_e32 v219, v219, v144
	v_mul_f32_e32 v204, v204, v145
	v_mul_f32_e32 v205, v205, v145
	v_mul_f32_e32 v220, v220, v145
	v_mul_f32_e32 v221, v221, v145
.Lq_ng_9:
	s_waitcnt lgkmcnt(14)
	v_cvt_pk_bf16_f32 v222, v190, v192
	s_waitcnt lgkmcnt(12)
	v_cvt_pk_bf16_f32 v223, v194, v196
	s_waitcnt lgkmcnt(10)
	v_cvt_pk_bf16_f32 v224, v198, v200
	s_waitcnt lgkmcnt(8)
	v_cvt_pk_bf16_f32 v225, v202, v204
	global_store_dwordx4 v170, v[222:225], s[18:19] nt
	v_cvt_pk_bf16_f32 v226, v191, v193
	v_cvt_pk_bf16_f32 v227, v195, v197
	v_cvt_pk_bf16_f32 v228, v199, v201
	v_cvt_pk_bf16_f32 v229, v203, v205
	global_store_dwordx4 v171, v[226:229], s[18:19] nt
	s_waitcnt lgkmcnt(6)
	v_cvt_pk_bf16_f32 v222, v206, v208
	s_waitcnt lgkmcnt(4)
	v_cvt_pk_bf16_f32 v223, v210, v212
	s_waitcnt lgkmcnt(2)
	v_cvt_pk_bf16_f32 v224, v214, v216
	s_waitcnt lgkmcnt(0)
	v_cvt_pk_bf16_f32 v225, v218, v220
	global_store_dwordx4 v172, v[222:225], s[18:19] nt
	v_cvt_pk_bf16_f32 v226, v207, v209
	v_cvt_pk_bf16_f32 v227, v211, v213
	v_cvt_pk_bf16_f32 v228, v215, v217
	v_cvt_pk_bf16_f32 v229, v219, v221
	global_store_dwordx4 v173, v[226:229], s[18:19] nt
	s_add_u32 s18, s6, 640
	s_addc_u32 s19, s7, 0
	s_nop 1
	global_load_dwordx4 v[34:37], v162, s[18:19] nt
	global_load_dwordx4 v[38:41], v163, s[18:19] nt
	global_load_dwordx4 v[42:45], v164, s[18:19] nt
	global_load_dwordx4 v[46:49], v165, s[18:19] nt
	global_load_dwordx4 v[50:53], v166, s[18:19] nt
	global_load_dwordx4 v[54:57], v167, s[18:19] nt
	global_load_dwordx4 v[58:61], v168, s[18:19] nt
	global_load_dwordx4 v[62:65], v169, s[18:19] nt
	global_load_dwordx4 v[138:141], v178, s[8:9]
	global_load_dwordx4 v[142:145], v178, s[8:9] offset:16
	s_bitcmp1_b32 s13, 0
	s_cselect_b32 s2, 2, 2
	s_mul_i32 s2, s2, s12
	s_add_u32 s18, s10, s2
	s_addc_u32 s19, s11, 0
	s_waitcnt vmcnt(51)
	ds_write2_b32 v180, v66, v67 offset1:1
	ds_write2_b32 v180, v68, v69 offset0:2 offset1:3
	s_waitcnt vmcnt(50)
	ds_write2_b32 v181, v70, v71 offset1:1
	ds_write2_b32 v181, v72, v73 offset0:2 offset1:3
	s_waitcnt vmcnt(49)
	ds_write2_b32 v182, v74, v75 offset1:1
	ds_write2_b32 v182, v76, v77 offset0:2 offset1:3
	s_waitcnt vmcnt(48)
	ds_write2_b32 v183, v78, v79 offset1:1
	ds_write2_b32 v183, v80, v81 offset0:2 offset1:3
	s_waitcnt vmcnt(47)
	ds_write2_b32 v184, v82, v83 offset1:1
	ds_write2_b32 v184, v84, v85 offset0:2 offset1:3
	s_waitcnt vmcnt(46)
	ds_write2_b32 v185, v86, v87 offset1:1
	ds_write2_b32 v185, v88, v89 offset0:2 offset1:3
	s_waitcnt vmcnt(45)
	ds_write2_b32 v186, v90, v91 offset1:1
	ds_write2_b32 v186, v92, v93 offset0:2 offset1:3
	s_waitcnt vmcnt(44)
	ds_write2_b32 v187, v94, v95 offset1:1
	ds_write2_b32 v187, v96, v97 offset0:2 offset1:3
	s_waitcnt lgkmcnt(0)
	ds_read2_b32 v[190:191], v188 offset0:0 offset1:8
	ds_read2_b32 v[192:193], v188 offset0:33 offset1:41
	ds_read2_b32 v[194:195], v188 offset0:66 offset1:74
	ds_read2_b32 v[196:197], v188 offset0:99 offset1:107
	ds_read2_b32 v[198:199], v188 offset0:132 offset1:140
	ds_read2_b32 v[200:201], v188 offset0:165 offset1:173
	ds_read2_b32 v[202:203], v188 offset0:198 offset1:206
	ds_read2_b32 v[204:205], v188 offset0:231 offset1:239
	ds_read2_b32 v[206:207], v188 offset0:16 offset1:24
	ds_read2_b32 v[208:209], v188 offset0:49 offset1:57
	ds_read2_b32 v[210:211], v188 offset0:82 offset1:90
	ds_read2_b32 v[212:213], v188 offset0:115 offset1:123
	ds_read2_b32 v[214:215], v188 offset0:148 offset1:156
	ds_read2_b32 v[216:217], v188 offset0:181 offset1:189
	ds_read2_b32 v[218:219], v188 offset0:214 offset1:222
	ds_read2_b32 v[220:221], v188 offset0:247 offset1:255
	s_bitcmp1_b32 s13, 1
	s_cbranch_scc0 .Lq_ng_10
	s_waitcnt vmcnt(42)
	s_waitcnt lgkmcnt(0)
	v_mul_f32_e32 v190, v190, v146
	v_mul_f32_e32 v191, v191, v146
	v_mul_f32_e32 v206, v206, v146
	v_mul_f32_e32 v207, v207, v146
	v_mul_f32_e32 v192, v192, v147
	v_mul_f32_e32 v193, v193, v147
	v_mul_f32_e32 v208, v208, v147
	v_mul_f32_e32 v209, v209, v147
	v_mul_f32_e32 v194, v194, v148
	v_mul_f32_e32 v195, v195, v148
	v_mul_f32_e32 v210, v210, v148
	v_mul_f32_e32 v211, v211, v148
	v_mul_f32_e32 v196, v196, v149
	v_mul_f32_e32 v197, v197, v149
	v_mul_f32_e32 v212, v212, v149
	v_mul_f32_e32 v213, v213, v149
	v_mul_f32_e32 v198, v198, v150
	v_mul_f32_e32 v199, v199, v150
	v_mul_f32_e32 v214, v214, v150
	v_mul_f32_e32 v215, v215, v150
	v_mul_f32_e32 v200, v200, v151
	v_mul_f32_e32 v201, v201, v151
	v_mul_f32_e32 v216, v216, v151
	v_mul_f32_e32 v217, v217, v151
	v_mul_f32_e32 v202, v202, v152
	v_mul_f32_e32 v203, v203, v152
	v_mul_f32_e32 v218, v218, v152
	v_mul_f32_e32 v219, v219, v152
	v_mul_f32_e32 v204, v204, v153
	v_mul_f32_e32 v205, v205, v153
	v_mul_f32_e32 v220, v220, v153
	v_mul_f32_e32 v221, v221, v153

.Lq_ng_11:
	s_waitcnt lgkmcnt(14)
	v_cvt_pk_bf16_f32 v222, v190, v192
	s_waitcnt lgkmcnt(12)
	v_cvt_pk_bf16_f32 v223, v194, v196
	s_waitcnt lgkmcnt(10)
	v_cvt_pk_bf16_f32 v224, v198, v200
	s_waitcnt lgkmcnt(8)
	v_cvt_pk_bf16_f32 v225, v202, v204
	global_store_dwordx4 v170, v[222:225], s[18:19] nt
	v_cvt_pk_bf16_f32 v226, v191, v193
	v_cvt_pk_bf16_f32 v227, v195, v197
	v_cvt_pk_bf16_f32 v228, v199, v201
	v_cvt_pk_bf16_f32 v229, v203, v205
	global_store_dwordx4 v171, v[226:229], s[18:19] nt
	s_waitcnt lgkmcnt(6)
	v_cvt_pk_bf16_f32 v222, v206, v208
	s_waitcnt lgkmcnt(4)
	v_cvt_pk_bf16_f32 v223, v210, v212
	s_waitcnt lgkmcnt(2)
	v_cvt_pk_bf16_f32 v224, v214, v216
	s_waitcnt lgkmcnt(0)
	v_cvt_pk_bf16_f32 v225, v218, v220
	global_store_dwordx4 v172, v[222:225], s[18:19] nt
	v_cvt_pk_bf16_f32 v226, v207, v209
	v_cvt_pk_bf16_f32 v227, v211, v213
	v_cvt_pk_bf16_f32 v228, v215, v217
	v_cvt_pk_bf16_f32 v229, v219, v221
	global_store_dwordx4 v173, v[226:229], s[18:19] nt
	s_add_u32 s18, s6, 896
	s_addc_u32 s19, s7, 0
	s_nop 1
	global_load_dwordx4 v[98:101], v162, s[18:19] nt
	global_load_dwordx4 v[102:105], v163, s[18:19] nt
	global_load_dwordx4 v[106:109], v164, s[18:19] nt
	global_load_dwordx4 v[110:113], v165, s[18:19] nt
	global_load_dwordx4 v[114:117], v166, s[18:19] nt
	global_load_dwordx4 v[118:121], v167, s[18:19] nt
	global_load_dwordx4 v[122:125], v168, s[18:19] nt
	global_load_dwordx4 v[126:129], v169, s[18:19] nt
	global_load_dwordx4 v[154:157], v178, s[8:9]
	global_load_dwordx4 v[158:161], v178, s[8:9] offset:16
	s_branch .Lq_loop
.Lq_drain:
	s_waitcnt vmcnt(0)
	s_bitcmp1_b32 s13, 0
	s_cselect_b32 s2, 8, 4
	s_mul_i32 s2, s2, s12
	s_add_u32 s18, s10, s2
	s_addc_u32 s19, s11, 0
	ds_write2_b32 v180, v2, v3 offset1:1
	ds_write2_b32 v180, v4, v5 offset0:2 offset1:3
	ds_write2_b32 v181, v6, v7 offset1:1
	ds_write2_b32 v181, v8, v9 offset0:2 offset1:3
	ds_write2_b32 v182, v10, v11 offset1:1
	ds_write2_b32 v182, v12, v13 offset0:2 offset1:3
	ds_write2_b32 v183, v14, v15 offset1:1
	ds_write2_b32 v183, v16, v17 offset0:2 offset1:3
	ds_write2_b32 v184, v18, v19 offset1:1
	ds_write2_b32 v184, v20, v21 offset0:2 offset1:3
	ds_write2_b32 v185, v22, v23 offset1:1
	ds_write2_b32 v185, v24, v25 offset0:2 offset1:3
	ds_write2_b32 v186, v26, v27 offset1:1
	ds_write2_b32 v186, v28, v29 offset0:2 offset1:3
	ds_write2_b32 v187, v30, v31 offset1:1
	ds_write2_b32 v187, v32, v33 offset0:2 offset1:3
	s_waitcnt lgkmcnt(0)
	ds_read2_b32 v[190:191], v188 offset0:0 offset1:8
	ds_read2_b32 v[192:193], v188 offset0:33 offset1:41
	ds_read2_b32 v[194:195], v188 offset0:66 offset1:74
	ds_read2_b32 v[196:197], v188 offset0:99 offset1:107
	ds_read2_b32 v[198:199], v188 offset0:132 offset1:140
	ds_read2_b32 v[200:201], v188 offset0:165 offset1:173
	ds_read2_b32 v[202:203], v188 offset0:198 offset1:206
	ds_read2_b32 v[204:205], v188 offset0:231 offset1:239
	ds_read2_b32 v[206:207], v188 offset0:16 offset1:24
	ds_read2_b32 v[208:209], v188 offset0:49 offset1:57
	ds_read2_b32 v[210:211], v188 offset0:82 offset1:90
	ds_read2_b32 v[212:213], v188 offset0:115 offset1:123
	ds_read2_b32 v[214:215], v188 offset0:148 offset1:156
	ds_read2_b32 v[216:217], v188 offset0:181 offset1:189
	ds_read2_b32 v[218:219], v188 offset0:214 offset1:222
	ds_read2_b32 v[220:221], v188 offset0:247 offset1:255
	s_bitcmp1_b32 s13, 1
	s_cbranch_scc0 .Lq_ng_12
	s_waitcnt lgkmcnt(0)
	v_mul_f32_e32 v190, v190, v130
	v_mul_f32_e32 v191, v191, v130
	v_mul_f32_e32 v206, v206, v130
	v_mul_f32_e32 v207, v207, v130
	v_mul_f32_e32 v192, v192, v131
	v_mul_f32_e32 v193, v193, v131
	v_mul_f32_e32 v208, v208, v131
	v_mul_f32_e32 v209, v209, v131
	v_mul_f32_e32 v194, v194, v132
	v_mul_f32_e32 v195, v195, v132
	v_mul_f32_e32 v210, v210, v132
	v_mul_f32_e32 v211, v211, v132
	v_mul_f32_e32 v196, v196, v133
	v_mul_f32_e32 v197, v197, v133
	v_mul_f32_e32 v212, v212, v133
	v_mul_f32_e32 v213, v213, v133
	v_mul_f32_e32 v198, v198, v134
	v_mul_f32_e32 v199, v199, v134
	v_mul_f32_e32 v214, v214, v134
	v_mul_f32_e32 v215, v215, v134
	v_mul_f32_e32 v200, v200, v135
	v_mul_f32_e32 v201, v201, v135
	v_mul_f32_e32 v216, v216, v135
	v_mul_f32_e32 v217, v217, v135
	v_mul_f32_e32 v202, v202, v136
	v_mul_f32_e32 v203, v203, v136
	v_mul_f32_e32 v218, v218, v136
	v_mul_f32_e32 v219, v219, v136
	v_mul_f32_e32 v204, v204, v137
	v_mul_f32_e32 v205, v205, v137
	v_mul_f32_e32 v220, v220, v137
	v_mul_f32_e32 v221, v221, v137
.Lq_ng_12:
	s_waitcnt lgkmcnt(14)
	v_cvt_pk_bf16_f32 v222, v190, v192
	s_waitcnt lgkmcnt(12)
	v_cvt_pk_bf16_f32 v223, v194, v196
	s_waitcnt lgkmcnt(10)
	v_cvt_pk_bf16_f32 v224, v198, v200
	s_waitcnt lgkmcnt(8)
	v_cvt_pk_bf16_f32 v225, v202, v204
	global_store_dwordx4 v170, v[222:225], s[18:19] nt
	v_cvt_pk_bf16_f32 v226, v191, v193
	v_cvt_pk_bf16_f32 v227, v195, v197
	v_cvt_pk_bf16_f32 v228, v199, v201
	v_cvt_pk_bf16_f32 v229, v203, v205
	global_store_dwordx4 v171, v[226:229], s[18:19] nt
	s_waitcnt lgkmcnt(6)
	v_cvt_pk_bf16_f32 v222, v206, v208
	s_waitcnt lgkmcnt(4)
	v_cvt_pk_bf16_f32 v223, v210, v212
	s_waitcnt lgkmcnt(2)
	v_cvt_pk_bf16_f32 v224, v214, v216
	s_waitcnt lgkmcnt(0)
	v_cvt_pk_bf16_f32 v225, v218, v220
	global_store_dwordx4 v172, v[222:225], s[18:19] nt
	v_cvt_pk_bf16_f32 v226, v207, v209
	v_cvt_pk_bf16_f32 v227, v211, v213
	v_cvt_pk_bf16_f32 v228, v215, v217
	v_cvt_pk_bf16_f32 v229, v219, v221
	global_store_dwordx4 v173, v[226:229], s[18:19] nt
	s_bitcmp1_b32 s13, 0
	s_cselect_b32 s2, 9, 5
	s_mul_i32 s2, s2, s12
	s_add_u32 s18, s10, s2
	s_addc_u32 s19, s11, 0
	ds_write2_b32 v180, v34, v35 offset1:1
	ds_write2_b32 v180, v36, v37 offset0:2 offset1:3
	ds_write2_b32 v181, v38, v39 offset1:1
	ds_write2_b32 v181, v40, v41 offset0:2 offset1:3
	ds_write2_b32 v182, v42, v43 offset1:1
	ds_write2_b32 v182, v44, v45 offset0:2 offset1:3
	ds_write2_b32 v183, v46, v47 offset1:1
	ds_write2_b32 v183, v48, v49 offset0:2 offset1:3
	ds_write2_b32 v184, v50, v51 offset1:1
	ds_write2_b32 v184, v52, v53 offset0:2 offset1:3
	ds_write2_b32 v185, v54, v55 offset1:1
	ds_write2_b32 v185, v56, v57 offset0:2 offset1:3
	ds_write2_b32 v186, v58, v59 offset1:1
	ds_write2_b32 v186, v60, v61 offset0:2 offset1:3
	ds_write2_b32 v187, v62, v63 offset1:1
	ds_write2_b32 v187, v64, v65 offset0:2 offset1:3
	s_waitcnt lgkmcnt(0)
	ds_read2_b32 v[190:191], v188 offset0:0 offset1:8
	ds_read2_b32 v[192:193], v188 offset0:33 offset1:41
	ds_read2_b32 v[194:195], v188 offset0:66 offset1:74
	ds_read2_b32 v[196:197], v188 offset0:99 offset1:107
	ds_read2_b32 v[198:199], v188 offset0:132 offset1:140
	ds_read2_b32 v[200:201], v188 offset0:165 offset1:173
	ds_read2_b32 v[202:203], v188 offset0:198 offset1:206
	ds_read2_b32 v[204:205], v188 offset0:231 offset1:239
	ds_read2_b32 v[206:207], v188 offset0:16 offset1:24
	ds_read2_b32 v[208:209], v188 offset0:49 offset1:57
	ds_read2_b32 v[210:211], v188 offset0:82 offset1:90
	ds_read2_b32 v[212:213], v188 offset0:115 offset1:123
	ds_read2_b32 v[214:215], v188 offset0:148 offset1:156
	ds_read2_b32 v[216:217], v188 offset0:181 offset1:189
	ds_read2_b32 v[218:219], v188 offset0:214 offset1:222
	ds_read2_b32 v[220:221], v188 offset0:247 offset1:255
	s_bitcmp1_b32 s13, 1
	s_cbranch_scc0 .Lq_ng_13
	s_waitcnt lgkmcnt(0)
	v_mul_f32_e32 v190, v190, v138
	v_mul_f32_e32 v191, v191, v138
	v_mul_f32_e32 v206, v206, v138
	v_mul_f32_e32 v207, v207, v138
	v_mul_f32_e32 v192, v192, v139
	v_mul_f32_e32 v193, v193, v139
	v_mul_f32_e32 v208, v208, v139
	v_mul_f32_e32 v209, v209, v139
	v_mul_f32_e32 v194, v194, v140
	v_mul_f32_e32 v195, v195, v140
	v_mul_f32_e32 v210, v210, v140
	v_mul_f32_e32 v211, v211, v140
	v_mul_f32_e32 v196, v196, v141
	v_mul_f32_e32 v197, v197, v141
	v_mul_f32_e32 v212, v212, v141
	v_mul_f32_e32 v213, v213, v141
	v_mul_f32_e32 v198, v198, v142
	v_mul_f32_e32 v199, v199, v142
	v_mul_f32_e32 v214, v214, v142
	v_mul_f32_e32 v215, v215, v142
	v_mul_f32_e32 v200, v200, v143
	v_mul_f32_e32 v201, v201, v143
	v_mul_f32_e32 v216, v216, v143
	v_mul_f32_e32 v217, v217, v143
	v_mul_f32_e32 v202, v202, v144
	v_mul_f32_e32 v203, v203, v144
	v_mul_f32_e32 v218, v218, v144
	v_mul_f32_e32 v219, v219, v144
	v_mul_f32_e32 v204, v204, v145
	v_mul_f32_e32 v205, v205, v145
	v_mul_f32_e32 v220, v220, v145
	v_mul_f32_e32 v221, v221, v145
.Lq_ng_13:
	s_waitcnt lgkmcnt(14)
	v_cvt_pk_bf16_f32 v222, v190, v192
	s_waitcnt lgkmcnt(12)
	v_cvt_pk_bf16_f32 v223, v194, v196
	s_waitcnt lgkmcnt(10)
	v_cvt_pk_bf16_f32 v224, v198, v200
	s_waitcnt lgkmcnt(8)
	v_cvt_pk_bf16_f32 v225, v202, v204
	global_store_dwordx4 v170, v[222:225], s[18:19] nt
	v_cvt_pk_bf16_f32 v226, v191, v193
	v_cvt_pk_bf16_f32 v227, v195, v197
	v_cvt_pk_bf16_f32 v228, v199, v201
	v_cvt_pk_bf16_f32 v229, v203, v205
	global_store_dwordx4 v171, v[226:229], s[18:19] nt
	s_waitcnt lgkmcnt(6)
	v_cvt_pk_bf16_f32 v222, v206, v208
	s_waitcnt lgkmcnt(4)
	v_cvt_pk_bf16_f32 v223, v210, v212
	s_waitcnt lgkmcnt(2)
	v_cvt_pk_bf16_f32 v224, v214, v216
	s_waitcnt lgkmcnt(0)
	v_cvt_pk_bf16_f32 v225, v218, v220
	global_store_dwordx4 v172, v[222:225], s[18:19] nt
	v_cvt_pk_bf16_f32 v226, v207, v209
	v_cvt_pk_bf16_f32 v227, v211, v213
	v_cvt_pk_bf16_f32 v228, v215, v217
	v_cvt_pk_bf16_f32 v229, v219, v221
	global_store_dwordx4 v173, v[226:229], s[18:19] nt
	s_bitcmp1_b32 s13, 0
	s_cselect_b32 s2, 10, 6
	s_mul_i32 s2, s2, s12
	s_add_u32 s18, s10, s2
	s_addc_u32 s19, s11, 0
	ds_write2_b32 v180, v66, v67 offset1:1
	ds_write2_b32 v180, v68, v69 offset0:2 offset1:3
	ds_write2_b32 v181, v70, v71 offset1:1
	ds_write2_b32 v181, v72, v73 offset0:2 offset1:3
	ds_write2_b32 v182, v74, v75 offset1:1
	ds_write2_b32 v182, v76, v77 offset0:2 offset1:3
	ds_write2_b32 v183, v78, v79 offset1:1
	ds_write2_b32 v183, v80, v81 offset0:2 offset1:3
	ds_write2_b32 v184, v82, v83 offset1:1
	ds_write2_b32 v184, v84, v85 offset0:2 offset1:3
	ds_write2_b32 v185, v86, v87 offset1:1
	ds_write2_b32 v185, v88, v89 offset0:2 offset1:3
	ds_write2_b32 v186, v90, v91 offset1:1
	ds_write2_b32 v186, v92, v93 offset0:2 offset1:3
	ds_write2_b32 v187, v94, v95 offset1:1
	ds_write2_b32 v187, v96, v97 offset0:2 offset1:3
	s_waitcnt lgkmcnt(0)
	ds_read2_b32 v[190:191], v188 offset0:0 offset1:8
	ds_read2_b32 v[192:193], v188 offset0:33 offset1:41
	ds_read2_b32 v[194:195], v188 offset0:66 offset1:74
	ds_read2_b32 v[196:197], v188 offset0:99 offset1:107
	ds_read2_b32 v[198:199], v188 offset0:132 offset1:140
	ds_read2_b32 v[200:201], v188 offset0:165 offset1:173
	ds_read2_b32 v[202:203], v188 offset0:198 offset1:206
	ds_read2_b32 v[204:205], v188 offset0:231 offset1:239
	ds_read2_b32 v[206:207], v188 offset0:16 offset1:24
	ds_read2_b32 v[208:209], v188 offset0:49 offset1:57
	ds_read2_b32 v[210:211], v188 offset0:82 offset1:90
	ds_read2_b32 v[212:213], v188 offset0:115 offset1:123
	ds_read2_b32 v[214:215], v188 offset0:148 offset1:156
	ds_read2_b32 v[216:217], v188 offset0:181 offset1:189
	ds_read2_b32 v[218:219], v188 offset0:214 offset1:222
	ds_read2_b32 v[220:221], v188 offset0:247 offset1:255
	s_bitcmp1_b32 s13, 1
	s_cbranch_scc0 .Lq_ng_14
	s_waitcnt lgkmcnt(0)
	v_mul_f32_e32 v190, v190, v146
	v_mul_f32_e32 v191, v191, v146
	v_mul_f32_e32 v206, v206, v146
	v_mul_f32_e32 v207, v207, v146
	v_mul_f32_e32 v192, v192, v147
	v_mul_f32_e32 v193, v193, v147
	v_mul_f32_e32 v208, v208, v147
	v_mul_f32_e32 v209, v209, v147
	v_mul_f32_e32 v194, v194, v148
	v_mul_f32_e32 v195, v195, v148
	v_mul_f32_e32 v210, v210, v148
	v_mul_f32_e32 v211, v211, v148
	v_mul_f32_e32 v196, v196, v149
	v_mul_f32_e32 v197, v197, v149
	v_mul_f32_e32 v212, v212, v149
	v_mul_f32_e32 v213, v213, v149
	v_mul_f32_e32 v198, v198, v150
	v_mul_f32_e32 v199, v199, v150
	v_mul_f32_e32 v214, v214, v150
	v_mul_f32_e32 v215, v215, v150
	v_mul_f32_e32 v200, v200, v151
	v_mul_f32_e32 v201, v201, v151
	v_mul_f32_e32 v216, v216, v151
	v_mul_f32_e32 v217, v217, v151
	v_mul_f32_e32 v202, v202, v152
	v_mul_f32_e32 v203, v203, v152
	v_mul_f32_e32 v218, v218, v152
	v_mul_f32_e32 v219, v219, v152
	v_mul_f32_e32 v204, v204, v153
	v_mul_f32_e32 v205, v205, v153
	v_mul_f32_e32 v220, v220, v153
	v_mul_f32_e32 v221, v221, v153
.Lq_ng_14:
	s_waitcnt lgkmcnt(14)
	v_cvt_pk_bf16_f32 v222, v190, v192
	s_waitcnt lgkmcnt(12)
	v_cvt_pk_bf16_f32 v223, v194, v196
	s_waitcnt lgkmcnt(10)
	v_cvt_pk_bf16_f32 v224, v198, v200
	s_waitcnt lgkmcnt(8)
	v_cvt_pk_bf16_f32 v225, v202, v204
	global_store_dwordx4 v170, v[222:225], s[18:19] nt
	v_cvt_pk_bf16_f32 v226, v191, v193
	v_cvt_pk_bf16_f32 v227, v195, v197
	v_cvt_pk_bf16_f32 v228, v199, v201
	v_cvt_pk_bf16_f32 v229, v203, v205
	global_store_dwordx4 v171, v[226:229], s[18:19] nt
	s_waitcnt lgkmcnt(6)
	v_cvt_pk_bf16_f32 v222, v206, v208
	s_waitcnt lgkmcnt(4)
	v_cvt_pk_bf16_f32 v223, v210, v212
	s_waitcnt lgkmcnt(2)
	v_cvt_pk_bf16_f32 v224, v214, v216
	s_waitcnt lgkmcnt(0)
	v_cvt_pk_bf16_f32 v225, v218, v220
	global_store_dwordx4 v172, v[222:225], s[18:19] nt
	v_cvt_pk_bf16_f32 v226, v207, v209
	v_cvt_pk_bf16_f32 v227, v211, v213
	v_cvt_pk_bf16_f32 v228, v215, v217
	v_cvt_pk_bf16_f32 v229, v219, v221
	global_store_dwordx4 v173, v[226:229], s[18:19] nt
	s_bitcmp1_b32 s13, 0
	s_cselect_b32 s2, 11, 7
	s_mul_i32 s2, s2, s12
	s_add_u32 s18, s10, s2
	s_addc_u32 s19, s11, 0
	ds_write2_b32 v180, v98, v99 offset1:1
	ds_write2_b32 v180, v100, v101 offset0:2 offset1:3
	ds_write2_b32 v181, v102, v103 offset1:1
	ds_write2_b32 v181, v104, v105 offset0:2 offset1:3
	ds_write2_b32 v182, v106, v107 offset1:1
	ds_write2_b32 v182, v108, v109 offset0:2 offset1:3
	ds_write2_b32 v183, v110, v111 offset1:1
	ds_write2_b32 v183, v112, v113 offset0:2 offset1:3
	ds_write2_b32 v184, v114, v115 offset1:1
	ds_write2_b32 v184, v116, v117 offset0:2 offset1:3
	ds_write2_b32 v185, v118, v119 offset1:1
	ds_write2_b32 v185, v120, v121 offset0:2 offset1:3
	ds_write2_b32 v186, v122, v123 offset1:1
	ds_write2_b32 v186, v124, v125 offset0:2 offset1:3
	ds_write2_b32 v187, v126, v127 offset1:1
	ds_write2_b32 v187, v128, v129 offset0:2 offset1:3
	s_waitcnt lgkmcnt(0)
	ds_read2_b32 v[190:191], v188 offset0:0 offset1:8
	ds_read2_b32 v[192:193], v188 offset0:33 offset1:41
	ds_read2_b32 v[194:195], v188 offset0:66 offset1:74
	ds_read2_b32 v[196:197], v188 offset0:99 offset1:107
	ds_read2_b32 v[198:199], v188 offset0:132 offset1:140
	ds_read2_b32 v[200:201], v188 offset0:165 offset1:173
	ds_read2_b32 v[202:203], v188 offset0:198 offset1:206
	ds_read2_b32 v[204:205], v188 offset0:231 offset1:239
	ds_read2_b32 v[206:207], v188 offset0:16 offset1:24
	ds_read2_b32 v[208:209], v188 offset0:49 offset1:57
	ds_read2_b32 v[210:211], v188 offset0:82 offset1:90
	ds_read2_b32 v[212:213], v188 offset0:115 offset1:123
	ds_read2_b32 v[214:215], v188 offset0:148 offset1:156
	ds_read2_b32 v[216:217], v188 offset0:181 offset1:189
	ds_read2_b32 v[218:219], v188 offset0:214 offset1:222
	ds_read2_b32 v[220:221], v188 offset0:247 offset1:255
	s_bitcmp1_b32 s13, 1
	s_cbranch_scc0 .Lq_ng_15
	s_waitcnt lgkmcnt(0)
	v_mul_f32_e32 v190, v190, v154
	v_mul_f32_e32 v191, v191, v154
	v_mul_f32_e32 v206, v206, v154
	v_mul_f32_e32 v207, v207, v154
	v_mul_f32_e32 v192, v192, v155
	v_mul_f32_e32 v193, v193, v155
	v_mul_f32_e32 v208, v208, v155
	v_mul_f32_e32 v209, v209, v155
	v_mul_f32_e32 v194, v194, v156
	v_mul_f32_e32 v195, v195, v156
	v_mul_f32_e32 v210, v210, v156
	v_mul_f32_e32 v211, v211, v156
	v_mul_f32_e32 v196, v196, v157
	v_mul_f32_e32 v197, v197, v157
	v_mul_f32_e32 v212, v212, v157
	v_mul_f32_e32 v213, v213, v157
	v_mul_f32_e32 v198, v198, v158
	v_mul_f32_e32 v199, v199, v158
	v_mul_f32_e32 v214, v214, v158
	v_mul_f32_e32 v215, v215, v158
	v_mul_f32_e32 v200, v200, v159
	v_mul_f32_e32 v201, v201, v159
	v_mul_f32_e32 v216, v216, v159
	v_mul_f32_e32 v217, v217, v159
	v_mul_f32_e32 v202, v202, v160
	v_mul_f32_e32 v203, v203, v160
	v_mul_f32_e32 v218, v218, v160
	v_mul_f32_e32 v219, v219, v160
	v_mul_f32_e32 v204, v204, v161
	v_mul_f32_e32 v205, v205, v161
	v_mul_f32_e32 v220, v220, v161
	v_mul_f32_e32 v221, v221, v161
.Lq_ng_15:
	s_waitcnt lgkmcnt(14)
	v_cvt_pk_bf16_f32 v222, v190, v192
	s_waitcnt lgkmcnt(12)
	v_cvt_pk_bf16_f32 v223, v194, v196
	s_waitcnt lgkmcnt(10)
	v_cvt_pk_bf16_f32 v224, v198, v200
	s_waitcnt lgkmcnt(8)
	v_cvt_pk_bf16_f32 v225, v202, v204
	global_store_dwordx4 v170, v[222:225], s[18:19] nt
	v_cvt_pk_bf16_f32 v226, v191, v193
	v_cvt_pk_bf16_f32 v227, v195, v197
	v_cvt_pk_bf16_f32 v228, v199, v201
	v_cvt_pk_bf16_f32 v229, v203, v205
	global_store_dwordx4 v171, v[226:229], s[18:19] nt
	s_waitcnt lgkmcnt(6)
	v_cvt_pk_bf16_f32 v222, v206, v208
	s_waitcnt lgkmcnt(4)
	v_cvt_pk_bf16_f32 v223, v210, v212
	s_waitcnt lgkmcnt(2)
	v_cvt_pk_bf16_f32 v224, v214, v216
	s_waitcnt lgkmcnt(0)
	v_cvt_pk_bf16_f32 v225, v218, v220
	global_store_dwordx4 v172, v[222:225], s[18:19] nt
	v_cvt_pk_bf16_f32 v226, v207, v209
	v_cvt_pk_bf16_f32 v227, v211, v213
	v_cvt_pk_bf16_f32 v228, v215, v217
	v_cvt_pk_bf16_f32 v229, v219, v221
	global_store_dwordx4 v173, v[226:229], s[18:19] nt
.Lq_exit:
	s_waitcnt vmcnt(0) lgkmcnt(0)
